# phase D layer 0: the 3x8 leftover units (65th row tile) spread over workgroups 0-23 instead of 0-7, MB chain kept by per-tile release/acquire counters in the zeroed control area
# baseline (speedup 1.0000x reference)
.LBB0_1199:
	ds_read_b128 v[142:145], v158
	ds_read_b128 v[162:165], v158 offset:1024
	ds_read_b128 v[166:169], v158 offset:2048
	ds_read_b128 v[170:173], v158 offset:3072
	s_add_u32 s26, s24, 0xfffc0080
	s_addc_u32 s27, s25, -1
	s_cmp_eq_u32 s56, 12
	s_cselect_b32 s29, s17, s27
	s_cselect_b32 s28, s52, s26
	s_cselect_b32 s27, s15, s55
	s_cselect_b32 s26, s53, s54
	v_lshl_add_u64 v[146:147], s[24:25], 0, v[134:135]
	s_add_i32 m0, s23, 0xc000
	ds_read_b128 v[174:177], v159
	ds_read_b128 v[178:181], v159 offset:1024
	ds_read_b128 v[182:185], v159 offset:2048
	ds_read_b128 v[186:189], v159 offset:3072
	ds_read_b128 v[192:195], v159 offset:4096
	ds_read_b128 v[196:199], v159 offset:5120
	ds_read_b128 v[200:203], v159 offset:6144
	ds_read_b128 v[204:207], v159 offset:7168
	global_load_lds_dwordx4 v[146:147], off
	v_lshl_add_u64 v[146:147], s[24:25], 0, v[136:137]
	s_add_i32 m0, s23, 0xe000
	s_nop 0
	global_load_lds_dwordx4 v[146:147], off
	s_waitcnt lgkmcnt(8)
	s_barrier
	s_waitcnt lgkmcnt(0)
	s_setprio 1
	s_waitcnt lgkmcnt(0)
	v_mfma_f32_16x16x32_bf16 v[126:129], v[142:145], v[174:177], v[126:129]
	v_mfma_f32_16x16x32_bf16 v[122:125], v[166:169], v[174:177], v[122:125]
	v_mfma_f32_16x16x32_bf16 v[114:117], v[142:145], v[182:185], v[114:117]
	v_mfma_f32_16x16x32_bf16 v[106:109], v[166:169], v[182:185], v[106:109]
	v_mfma_f32_16x16x32_bf16 v[98:101], v[142:145], v[192:195], v[98:101]
	v_mfma_f32_16x16x32_bf16 v[90:93], v[166:169], v[192:195], v[90:93]
	v_mfma_f32_16x16x32_bf16 v[82:85], v[142:145], v[200:203], v[82:85]
	v_mfma_f32_16x16x32_bf16 v[74:77], v[166:169], v[200:203], v[74:77]
	v_mfma_f32_16x16x32_bf16 v[126:129], v[162:165], v[178:181], v[126:129]
	v_mfma_f32_16x16x32_bf16 v[122:125], v[170:173], v[178:181], v[122:125]
	v_mfma_f32_16x16x32_bf16 v[114:117], v[162:165], v[186:189], v[114:117]
	v_mfma_f32_16x16x32_bf16 v[106:109], v[170:173], v[186:189], v[106:109]
	v_mfma_f32_16x16x32_bf16 v[98:101], v[162:165], v[196:199], v[98:101]
	v_mfma_f32_16x16x32_bf16 v[90:93], v[170:173], v[196:199], v[90:93]
	v_mfma_f32_16x16x32_bf16 v[82:85], v[162:165], v[204:207], v[82:85]
	v_mfma_f32_16x16x32_bf16 v[74:77], v[170:173], v[204:207], v[74:77]
	s_setprio 0
	s_barrier
	s_add_i32 s57, s48, s38
	v_lshl_add_u64 v[146:147], s[26:27], 0, v[130:131]
	s_mov_b32 m0, s57
	ds_read_b128 v[208:211], v160
	ds_read_b128 v[212:215], v160 offset:1024
	ds_read_b128 v[216:219], v160 offset:2048
	ds_read_b128 v[220:223], v160 offset:3072
	global_load_lds_dwordx4 v[146:147], off
	v_lshl_add_u64 v[190:191], s[26:27], 0, v[132:133]
	s_add_i32 m0, s57, 0x2000
	s_nop 0
	global_load_lds_dwordx4 v[190:191], off
	s_barrier
	s_waitcnt lgkmcnt(0)
	s_setprio 1
	s_waitcnt lgkmcnt(0)
	v_mfma_f32_16x16x32_bf16 v[118:121], v[208:211], v[174:177], v[118:121]
	v_mfma_f32_16x16x32_bf16 v[110:113], v[216:219], v[174:177], v[110:113]
	v_mfma_f32_16x16x32_bf16 v[102:105], v[208:211], v[182:185], v[102:105]
	v_mfma_f32_16x16x32_bf16 v[94:97], v[216:219], v[182:185], v[94:97]
	v_mfma_f32_16x16x32_bf16 v[86:89], v[208:211], v[192:195], v[86:89]
	v_mfma_f32_16x16x32_bf16 v[78:81], v[216:219], v[192:195], v[78:81]
	v_mfma_f32_16x16x32_bf16 v[70:73], v[208:211], v[200:203], v[70:73]
	v_mfma_f32_16x16x32_bf16 v[66:69], v[216:219], v[200:203], v[66:69]
	v_mfma_f32_16x16x32_bf16 v[118:121], v[212:215], v[178:181], v[118:121]
	v_mfma_f32_16x16x32_bf16 v[110:113], v[220:223], v[178:181], v[110:113]
	v_mfma_f32_16x16x32_bf16 v[102:105], v[212:215], v[186:189], v[102:105]
	v_mfma_f32_16x16x32_bf16 v[94:97], v[220:223], v[186:189], v[94:97]
	v_mfma_f32_16x16x32_bf16 v[86:89], v[212:215], v[196:199], v[86:89]
	v_mfma_f32_16x16x32_bf16 v[78:81], v[220:223], v[196:199], v[78:81]
	v_mfma_f32_16x16x32_bf16 v[70:73], v[212:215], v[204:207], v[70:73]
	v_mfma_f32_16x16x32_bf16 v[66:69], v[220:223], v[204:207], v[66:69]
	s_setprio 0
	s_mov_b32 m0, s23
	v_lshl_add_u64 v[224:225], s[28:29], 0, v[130:131]
	s_barrier
	ds_read_b128 v[174:177], v159 offset:16384
	ds_read_b128 v[178:181], v159 offset:17408
	ds_read_b128 v[182:185], v159 offset:18432
	ds_read_b128 v[186:189], v159 offset:19456
	ds_read_b128 v[192:195], v159 offset:20480
	ds_read_b128 v[196:199], v159 offset:21504
	ds_read_b128 v[200:203], v159 offset:22528
	ds_read_b128 v[204:207], v159 offset:23552
	global_load_lds_dwordx4 v[224:225], off
	v_lshl_add_u64 v[226:227], s[28:29], 0, v[132:133]
	s_mov_b32 m0, s41
	s_nop 0
	global_load_lds_dwordx4 v[226:227], off
	s_barrier
	s_waitcnt lgkmcnt(0)
	s_setprio 1
	s_waitcnt lgkmcnt(0)
	v_mfma_f32_16x16x32_bf16 v[62:65], v[142:145], v[174:177], v[62:65]
	v_mfma_f32_16x16x32_bf16 v[58:61], v[166:169], v[174:177], v[58:61]
	v_mfma_f32_16x16x32_bf16 v[50:53], v[142:145], v[182:185], v[50:53]
	v_mfma_f32_16x16x32_bf16 v[42:45], v[166:169], v[182:185], v[42:45]
	v_mfma_f32_16x16x32_bf16 v[34:37], v[142:145], v[192:195], v[34:37]
	v_mfma_f32_16x16x32_bf16 v[26:29], v[166:169], v[192:195], v[26:29]
	v_mfma_f32_16x16x32_bf16 v[18:21], v[142:145], v[200:203], v[18:21]
	v_mfma_f32_16x16x32_bf16 v[10:13], v[166:169], v[200:203], v[10:13]
	v_mfma_f32_16x16x32_bf16 v[62:65], v[162:165], v[178:181], v[62:65]
	v_mfma_f32_16x16x32_bf16 v[58:61], v[170:173], v[178:181], v[58:61]
	v_mfma_f32_16x16x32_bf16 v[50:53], v[162:165], v[186:189], v[50:53]
	v_mfma_f32_16x16x32_bf16 v[42:45], v[170:173], v[186:189], v[42:45]
	v_mfma_f32_16x16x32_bf16 v[34:37], v[162:165], v[196:199], v[34:37]
	v_mfma_f32_16x16x32_bf16 v[26:29], v[170:173], v[196:199], v[26:29]
	v_mfma_f32_16x16x32_bf16 v[18:21], v[162:165], v[204:207], v[18:21]
	v_mfma_f32_16x16x32_bf16 v[10:13], v[170:173], v[204:207], v[10:13]
	s_setprio 0
	s_barrier
	s_add_u32 s58, s26, 0x40000
	s_addc_u32 s59, s27, 0
	s_add_i32 s57, s49, s38
	v_lshl_add_u64 v[142:143], s[58:59], 0, v[130:131]
	s_mov_b32 m0, s57
	s_nop 0
	global_load_lds_dwordx4 v[142:143], off
	v_lshl_add_u64 v[142:143], s[58:59], 0, v[132:133]
	s_add_i32 m0, s57, 0x2000
	s_nop 0
	global_load_lds_dwordx4 v[142:143], off
	s_waitcnt vmcnt(6)
	s_barrier
	s_setprio 1
	v_mfma_f32_16x16x32_bf16 v[54:57], v[208:211], v[174:177], v[54:57]
	v_mfma_f32_16x16x32_bf16 v[46:49], v[216:219], v[174:177], v[46:49]
	v_mfma_f32_16x16x32_bf16 v[38:41], v[208:211], v[182:185], v[38:41]
	v_mfma_f32_16x16x32_bf16 v[30:33], v[216:219], v[182:185], v[30:33]
	v_mfma_f32_16x16x32_bf16 v[22:25], v[208:211], v[192:195], v[22:25]
	v_mfma_f32_16x16x32_bf16 v[14:17], v[216:219], v[192:195], v[14:17]
	v_mfma_f32_16x16x32_bf16 v[6:9], v[208:211], v[200:203], v[6:9]
	v_mfma_f32_16x16x32_bf16 v[2:5], v[216:219], v[200:203], v[2:5]
	v_mfma_f32_16x16x32_bf16 v[54:57], v[212:215], v[178:181], v[54:57]
	v_mfma_f32_16x16x32_bf16 v[46:49], v[220:223], v[178:181], v[46:49]
	v_mfma_f32_16x16x32_bf16 v[38:41], v[212:215], v[186:189], v[38:41]
	v_mfma_f32_16x16x32_bf16 v[30:33], v[220:223], v[186:189], v[30:33]
	v_mfma_f32_16x16x32_bf16 v[22:25], v[212:215], v[196:199], v[22:25]
	v_mfma_f32_16x16x32_bf16 v[14:17], v[220:223], v[196:199], v[14:17]
	v_mfma_f32_16x16x32_bf16 v[6:9], v[212:215], v[204:207], v[6:9]
	v_mfma_f32_16x16x32_bf16 v[2:5], v[220:223], v[204:207], v[2:5]
	s_setprio 0
	s_add_i32 s57, 0, 0x18000
	v_add_u32_e32 v161, s57, v156
	s_barrier
	ds_read_b128 v[142:145], v161
	ds_read_b128 v[162:165], v161 offset:1024
	ds_read_b128 v[166:169], v161 offset:2048
	ds_read_b128 v[170:173], v161 offset:3072
	s_add_u32 s28, s28, 0x40000
	s_addc_u32 s29, s29, 0
	s_mov_b32 m0, s42
	v_lshl_add_u64 v[208:209], s[28:29], 0, v[130:131]
	ds_read_b128 v[174:177], v159 offset:32768
	ds_read_b128 v[178:181], v159 offset:33792
	ds_read_b128 v[182:185], v159 offset:34816
	ds_read_b128 v[186:189], v159 offset:35840
	ds_read_b128 v[192:195], v159 offset:36864
	ds_read_b128 v[196:199], v159 offset:37888
	ds_read_b128 v[200:203], v159 offset:38912
	ds_read_b128 v[204:207], v159 offset:39936
	global_load_lds_dwordx4 v[208:209], off
	v_lshl_add_u64 v[208:209], s[28:29], 0, v[132:133]
	s_mov_b32 m0, s43
	s_nop 0
	global_load_lds_dwordx4 v[208:209], off
	s_waitcnt lgkmcnt(8)
	s_barrier
	s_waitcnt lgkmcnt(0)
	s_setprio 1
	s_waitcnt lgkmcnt(0)
	v_mfma_f32_16x16x32_bf16 v[126:129], v[142:145], v[174:177], v[126:129]
	v_mfma_f32_16x16x32_bf16 v[122:125], v[166:169], v[174:177], v[122:125]
	v_mfma_f32_16x16x32_bf16 v[114:117], v[142:145], v[182:185], v[114:117]
	v_mfma_f32_16x16x32_bf16 v[106:109], v[166:169], v[182:185], v[106:109]
	v_mfma_f32_16x16x32_bf16 v[98:101], v[142:145], v[192:195], v[98:101]
	v_mfma_f32_16x16x32_bf16 v[90:93], v[166:169], v[192:195], v[90:93]
	v_mfma_f32_16x16x32_bf16 v[82:85], v[142:145], v[200:203], v[82:85]
	v_mfma_f32_16x16x32_bf16 v[74:77], v[166:169], v[200:203], v[74:77]
	v_mfma_f32_16x16x32_bf16 v[126:129], v[162:165], v[178:181], v[126:129]
	v_mfma_f32_16x16x32_bf16 v[122:125], v[170:173], v[178:181], v[122:125]
	v_mfma_f32_16x16x32_bf16 v[114:117], v[162:165], v[186:189], v[114:117]
	v_mfma_f32_16x16x32_bf16 v[106:109], v[170:173], v[186:189], v[106:109]
	v_mfma_f32_16x16x32_bf16 v[98:101], v[162:165], v[196:199], v[98:101]
	v_mfma_f32_16x16x32_bf16 v[90:93], v[170:173], v[196:199], v[90:93]
	v_mfma_f32_16x16x32_bf16 v[82:85], v[162:165], v[204:207], v[82:85]
	v_mfma_f32_16x16x32_bf16 v[74:77], v[170:173], v[204:207], v[74:77]
	s_setprio 0
	s_barrier
	s_add_i32 s28, 0, 0x1c000
	s_add_i32 s29, s57, s38
	v_add_u32_e32 v161, s28, v156
	v_lshl_add_u64 v[146:147], v[146:147], 0, s[8:9]
	s_mov_b32 m0, s29
	ds_read_b128 v[208:211], v161
	ds_read_b128 v[212:215], v161 offset:1024
	ds_read_b128 v[216:219], v161 offset:2048
	ds_read_b128 v[220:223], v161 offset:3072
	global_load_lds_dwordx4 v[146:147], off
	v_lshl_add_u64 v[146:147], v[190:191], 0, s[8:9]
	s_add_i32 m0, s29, 0x2000
	s_nop 0
	global_load_lds_dwordx4 v[146:147], off
	s_barrier
	s_waitcnt lgkmcnt(0)
	s_setprio 1
	s_waitcnt lgkmcnt(0)
	v_mfma_f32_16x16x32_bf16 v[118:121], v[208:211], v[174:177], v[118:121]
	v_mfma_f32_16x16x32_bf16 v[110:113], v[216:219], v[174:177], v[110:113]
	v_mfma_f32_16x16x32_bf16 v[102:105], v[208:211], v[182:185], v[102:105]
	v_mfma_f32_16x16x32_bf16 v[94:97], v[216:219], v[182:185], v[94:97]
	v_mfma_f32_16x16x32_bf16 v[86:89], v[208:211], v[192:195], v[86:89]
	v_mfma_f32_16x16x32_bf16 v[78:81], v[216:219], v[192:195], v[78:81]
	v_mfma_f32_16x16x32_bf16 v[70:73], v[208:211], v[200:203], v[70:73]
	v_mfma_f32_16x16x32_bf16 v[66:69], v[216:219], v[200:203], v[66:69]
	v_mfma_f32_16x16x32_bf16 v[118:121], v[212:215], v[178:181], v[118:121]
	v_mfma_f32_16x16x32_bf16 v[110:113], v[220:223], v[178:181], v[110:113]
	v_mfma_f32_16x16x32_bf16 v[102:105], v[212:215], v[186:189], v[102:105]
	v_mfma_f32_16x16x32_bf16 v[94:97], v[220:223], v[186:189], v[94:97]
	v_mfma_f32_16x16x32_bf16 v[86:89], v[212:215], v[196:199], v[86:89]
	v_mfma_f32_16x16x32_bf16 v[78:81], v[220:223], v[196:199], v[78:81]
	v_mfma_f32_16x16x32_bf16 v[70:73], v[212:215], v[204:207], v[70:73]
	v_mfma_f32_16x16x32_bf16 v[66:69], v[220:223], v[204:207], v[66:69]
	s_setprio 0
	s_mov_b32 m0, s45
	v_lshl_add_u64 v[146:147], v[224:225], 0, s[8:9]
	s_barrier
	ds_read_b128 v[174:177], v159 offset:49152
	ds_read_b128 v[178:181], v159 offset:50176
	ds_read_b128 v[182:185], v159 offset:51200
	ds_read_b128 v[186:189], v159 offset:52224
	ds_read_b128 v[192:195], v159 offset:53248
	ds_read_b128 v[196:199], v159 offset:54272
	ds_read_b128 v[200:203], v159 offset:55296
	ds_read_b128 v[204:207], v159 offset:56320
	global_load_lds_dwordx4 v[146:147], off
	v_lshl_add_u64 v[146:147], v[226:227], 0, s[8:9]
	s_mov_b32 m0, s46
	s_nop 0
	global_load_lds_dwordx4 v[146:147], off
	s_barrier
	s_waitcnt lgkmcnt(0)
	s_setprio 1
	s_waitcnt lgkmcnt(0)
	v_mfma_f32_16x16x32_bf16 v[62:65], v[142:145], v[174:177], v[62:65]
	v_mfma_f32_16x16x32_bf16 v[58:61], v[166:169], v[174:177], v[58:61]
	v_mfma_f32_16x16x32_bf16 v[50:53], v[142:145], v[182:185], v[50:53]
	v_mfma_f32_16x16x32_bf16 v[42:45], v[166:169], v[182:185], v[42:45]
	v_mfma_f32_16x16x32_bf16 v[34:37], v[142:145], v[192:195], v[34:37]
	v_mfma_f32_16x16x32_bf16 v[26:29], v[166:169], v[192:195], v[26:29]
	v_mfma_f32_16x16x32_bf16 v[18:21], v[142:145], v[200:203], v[18:21]
	v_mfma_f32_16x16x32_bf16 v[10:13], v[166:169], v[200:203], v[10:13]
	v_mfma_f32_16x16x32_bf16 v[62:65], v[162:165], v[178:181], v[62:65]
	v_mfma_f32_16x16x32_bf16 v[58:61], v[170:173], v[178:181], v[58:61]
	v_mfma_f32_16x16x32_bf16 v[50:53], v[162:165], v[186:189], v[50:53]
	v_mfma_f32_16x16x32_bf16 v[42:45], v[170:173], v[186:189], v[42:45]
	v_mfma_f32_16x16x32_bf16 v[34:37], v[162:165], v[196:199], v[34:37]
	v_mfma_f32_16x16x32_bf16 v[26:29], v[170:173], v[196:199], v[26:29]
	v_mfma_f32_16x16x32_bf16 v[18:21], v[162:165], v[204:207], v[18:21]
	v_mfma_f32_16x16x32_bf16 v[10:13], v[170:173], v[204:207], v[10:13]
	s_setprio 0
	s_barrier
	s_add_u32 s26, s26, 0x40080
	s_addc_u32 s27, s27, 0
	s_add_i32 s28, s28, s38
	v_lshl_add_u64 v[142:143], s[26:27], 0, v[130:131]
	s_mov_b32 m0, s28
	s_nop 0
	global_load_lds_dwordx4 v[142:143], off
	v_lshl_add_u64 v[142:143], s[26:27], 0, v[132:133]
	s_add_i32 m0, s28, 0x2000
	s_nop 0
	global_load_lds_dwordx4 v[142:143], off
	s_waitcnt vmcnt(6)
	s_barrier
	s_setprio 1
	v_mfma_f32_16x16x32_bf16 v[54:57], v[208:211], v[174:177], v[54:57]
	v_mfma_f32_16x16x32_bf16 v[46:49], v[216:219], v[174:177], v[46:49]
	v_mfma_f32_16x16x32_bf16 v[38:41], v[208:211], v[182:185], v[38:41]
	v_mfma_f32_16x16x32_bf16 v[30:33], v[216:219], v[182:185], v[30:33]
	v_mfma_f32_16x16x32_bf16 v[22:25], v[208:211], v[192:195], v[22:25]
	v_mfma_f32_16x16x32_bf16 v[14:17], v[216:219], v[192:195], v[14:17]
	v_mfma_f32_16x16x32_bf16 v[6:9], v[208:211], v[200:203], v[6:9]
	v_mfma_f32_16x16x32_bf16 v[2:5], v[216:219], v[200:203], v[2:5]
	v_mfma_f32_16x16x32_bf16 v[54:57], v[212:215], v[178:181], v[54:57]
	v_mfma_f32_16x16x32_bf16 v[46:49], v[220:223], v[178:181], v[46:49]
	v_mfma_f32_16x16x32_bf16 v[38:41], v[212:215], v[186:189], v[38:41]
	v_mfma_f32_16x16x32_bf16 v[30:33], v[220:223], v[186:189], v[30:33]
	v_mfma_f32_16x16x32_bf16 v[22:25], v[212:215], v[196:199], v[22:25]
	v_mfma_f32_16x16x32_bf16 v[14:17], v[220:223], v[196:199], v[14:17]
	v_mfma_f32_16x16x32_bf16 v[6:9], v[212:215], v[204:207], v[6:9]
	v_mfma_f32_16x16x32_bf16 v[2:5], v[220:223], v[204:207], v[2:5]
	s_setprio 0
	s_add_i32 s56, s56, 2
	s_add_u32 s24, s24, 0x100
	s_addc_u32 s25, s25, 0
	s_add_u32 s54, s54, 0x100
	s_addc_u32 s55, s55, 0
	s_cmp_gt_u32 s56, 13
	s_barrier
	s_cbranch_scc0 .LBB0_1199
	v_lshl_or_b32 v142, s51, 8, v157
	v_lshl_add_u32 v144, s22, 8, v155
	v_ashrrev_i32_e32 v143, 31, v142
	v_mov_b64_e32 v[146:147], s[10:11]
	v_mad_i64_i32 v[162:163], s[24:25], v144, s50, v[146:147]
	v_lshlrev_b64 v[142:143], 1, v[142:143]
	v_lshl_add_u64 v[162:163], v[162:163], 0, v[142:143]
	v_mov_b32_e32 v238, v162
	v_mov_b32_e32 v239, v163
	global_load_dwordx2 v[168:169], v[238:239], off
	global_load_dwordx2 v[170:171], v[238:239], off offset:32
	global_load_dwordx2 v[172:173], v[238:239], off offset:256
	global_load_dwordx2 v[174:175], v[238:239], off offset:288
	v_mov_b32_e32 v242, 16
	v_mad_i64_i32 v[240:241], s[24:25], v242, s50, v[238:239]
	global_load_dwordx2 v[176:177], v[240:241], off
	global_load_dwordx2 v[178:179], v[240:241], off offset:32
	global_load_dwordx2 v[180:181], v[240:241], off offset:256
	global_load_dwordx2 v[182:183], v[240:241], off offset:288
	v_mov_b32_e32 v242, 32
	v_mad_i64_i32 v[240:241], s[24:25], v242, s50, v[238:239]
	global_load_dwordx2 v[184:185], v[240:241], off
	global_load_dwordx2 v[186:187], v[240:241], off offset:32
	global_load_dwordx2 v[188:189], v[240:241], off offset:256
	global_load_dwordx2 v[192:193], v[240:241], off offset:288
	v_mov_b32_e32 v242, 48
	v_mad_i64_i32 v[240:241], s[24:25], v242, s50, v[238:239]
	global_load_dwordx2 v[194:195], v[240:241], off
	global_load_dwordx2 v[196:197], v[240:241], off offset:32
	global_load_dwordx2 v[198:199], v[240:241], off offset:256
	global_load_dwordx2 v[200:201], v[240:241], off offset:288
	v_mov_b32_e32 v242, 128
	v_mad_i64_i32 v[240:241], s[24:25], v242, s50, v[238:239]
	global_load_dwordx2 v[202:203], v[240:241], off
	global_load_dwordx2 v[204:205], v[240:241], off offset:32
	global_load_dwordx2 v[206:207], v[240:241], off offset:256
	global_load_dwordx2 v[208:209], v[240:241], off offset:288
	v_mov_b32_e32 v242, 144
	v_mad_i64_i32 v[240:241], s[24:25], v242, s50, v[238:239]
	global_load_dwordx2 v[210:211], v[240:241], off
	global_load_dwordx2 v[212:213], v[240:241], off offset:32
	global_load_dwordx2 v[214:215], v[240:241], off offset:256
	global_load_dwordx2 v[216:217], v[240:241], off offset:288
	v_mov_b32_e32 v242, 160
	v_mad_i64_i32 v[240:241], s[24:25], v242, s50, v[238:239]
	global_load_dwordx2 v[218:219], v[240:241], off
	global_load_dwordx2 v[220:221], v[240:241], off offset:32
	global_load_dwordx2 v[222:223], v[240:241], off offset:256
	global_load_dwordx2 v[228:229], v[240:241], off offset:288
	v_mov_b32_e32 v242, 176
	v_mad_i64_i32 v[240:241], s[24:25], v242, s50, v[238:239]
	global_load_dwordx2 v[230:231], v[240:241], off
	global_load_dwordx2 v[232:233], v[240:241], off offset:32
	global_load_dwordx2 v[234:235], v[240:241], off offset:256
	global_load_dwordx2 v[236:237], v[240:241], off offset:288
	s_waitcnt vmcnt(0)
	v_mov_b32_e32 v164, v168
	v_mov_b32_e32 v165, v169
	v_ashrrev_i32_e32 v145, 31, v144
	s_and_b64 vcc, exec, s[0:1]
	s_mov_b32 s51, s14
	s_mov_b32 s22, s16
	s_mov_b64 s[26:27], s[20:21]
	s_nop 0
	v_lshlrev_b32_e32 v166, 16, v164
	v_and_b32_e32 v167, 0xffff0000, v164
	v_lshlrev_b32_e32 v164, 16, v165
	v_and_b32_e32 v165, 0xffff0000, v165
	v_pk_mul_f32 v[128:129], v[128:129], v[164:165]
	v_pk_mul_f32 v[126:127], v[126:127], v[166:167]
	v_lshlrev_b64 v[164:165], 12, v[144:145]
	v_cvt_pk_bf16_f32 v126, v126, v127
	v_cvt_pk_bf16_f32 v127, v128, v129
	v_mov_b32_e32 v128, v170
	v_mov_b32_e32 v129, v171
	v_lshl_add_u64 v[164:165], s[12:13], 0, v[164:165]
	v_lshl_add_u64 v[164:165], v[164:165], 0, v[142:143]
	global_store_dwordx2 v[164:165], v[126:127], off
	s_nop 0
	v_lshlrev_b32_e32 v126, 16, v128
	v_and_b32_e32 v127, 0xffff0000, v128
	v_lshlrev_b32_e32 v128, 16, v129
	v_and_b32_e32 v129, 0xffff0000, v129
	v_pk_mul_f32 v[124:125], v[124:125], v[128:129]
	v_pk_mul_f32 v[122:123], v[122:123], v[126:127]
	s_nop 0
	v_cvt_pk_bf16_f32 v122, v122, v123
	v_cvt_pk_bf16_f32 v123, v124, v125
	v_mov_b32_e32 v124, v172
	v_mov_b32_e32 v125, v173
	s_nop 0
	global_store_dwordx2 v[164:165], v[122:123], off offset:32
	s_nop 0
	v_lshlrev_b32_e32 v122, 16, v124
	v_and_b32_e32 v123, 0xffff0000, v124
	v_lshlrev_b32_e32 v124, 16, v125
	v_and_b32_e32 v125, 0xffff0000, v125
	v_pk_mul_f32 v[120:121], v[120:121], v[124:125]
	v_pk_mul_f32 v[118:119], v[118:119], v[122:123]
	v_or_b32_e32 v122, 16, v144
	v_cvt_pk_bf16_f32 v118, v118, v119
	v_cvt_pk_bf16_f32 v119, v120, v121
	v_mov_b32_e32 v120, v174
	v_mov_b32_e32 v121, v175
	v_mad_i64_i32 v[124:125], s[24:25], v122, s50, v[146:147]
	global_store_dwordx2 v[164:165], v[118:119], off offset:256
	v_lshl_add_u64 v[124:125], v[124:125], 0, v[142:143]
	v_ashrrev_i32_e32 v123, 31, v122
	s_nop 0
	v_lshlrev_b32_e32 v118, 16, v120
	v_and_b32_e32 v119, 0xffff0000, v120
	v_lshlrev_b32_e32 v120, 16, v121
	v_and_b32_e32 v121, 0xffff0000, v121
	v_pk_mul_f32 v[112:113], v[112:113], v[120:121]
	v_pk_mul_f32 v[110:111], v[110:111], v[118:119]
	s_nop 0
	v_cvt_pk_bf16_f32 v110, v110, v111
	v_cvt_pk_bf16_f32 v111, v112, v113
	v_mov_b32_e32 v112, v176
	v_mov_b32_e32 v113, v177
	s_nop 0
	global_store_dwordx2 v[164:165], v[110:111], off offset:288
	s_nop 0
	v_lshlrev_b32_e32 v110, 16, v112
	v_and_b32_e32 v111, 0xffff0000, v112
	v_lshlrev_b32_e32 v112, 16, v113
	v_and_b32_e32 v113, 0xffff0000, v113
	v_pk_mul_f32 v[112:113], v[116:117], v[112:113]
	v_pk_mul_f32 v[110:111], v[114:115], v[110:111]
	v_lshlrev_b64 v[114:115], 12, v[122:123]
	v_cvt_pk_bf16_f32 v110, v110, v111
	v_cvt_pk_bf16_f32 v111, v112, v113
	v_mov_b32_e32 v112, v178
	v_mov_b32_e32 v113, v179
	v_lshl_add_u64 v[114:115], s[12:13], 0, v[114:115]
	v_lshl_add_u64 v[114:115], v[114:115], 0, v[142:143]
	global_store_dwordx2 v[114:115], v[110:111], off
	s_nop 0
	v_lshlrev_b32_e32 v110, 16, v112
	v_and_b32_e32 v111, 0xffff0000, v112
	v_lshlrev_b32_e32 v112, 16, v113
	v_and_b32_e32 v113, 0xffff0000, v113
	v_pk_mul_f32 v[108:109], v[108:109], v[112:113]
	v_pk_mul_f32 v[106:107], v[106:107], v[110:111]
	s_nop 0
	v_cvt_pk_bf16_f32 v106, v106, v107
	v_cvt_pk_bf16_f32 v107, v108, v109
	v_mov_b32_e32 v108, v180
	v_mov_b32_e32 v109, v181
	s_nop 0
	global_store_dwordx2 v[114:115], v[106:107], off offset:32
	s_nop 0
	v_lshlrev_b32_e32 v106, 16, v108
	v_and_b32_e32 v107, 0xffff0000, v108
	v_lshlrev_b32_e32 v108, 16, v109
	v_and_b32_e32 v109, 0xffff0000, v109
	v_pk_mul_f32 v[104:105], v[104:105], v[108:109]
	v_pk_mul_f32 v[102:103], v[102:103], v[106:107]
	v_or_b32_e32 v106, 32, v144
	v_cvt_pk_bf16_f32 v102, v102, v103
	v_cvt_pk_bf16_f32 v103, v104, v105
	v_mov_b32_e32 v104, v182
	v_mov_b32_e32 v105, v183
	v_mad_i64_i32 v[108:109], s[24:25], v106, s50, v[146:147]
	global_store_dwordx2 v[114:115], v[102:103], off offset:256
	v_lshl_add_u64 v[108:109], v[108:109], 0, v[142:143]
	v_ashrrev_i32_e32 v107, 31, v106
	s_nop 0
	v_lshlrev_b32_e32 v102, 16, v104
	v_and_b32_e32 v103, 0xffff0000, v104
	v_lshlrev_b32_e32 v104, 16, v105
	v_and_b32_e32 v105, 0xffff0000, v105
	v_pk_mul_f32 v[96:97], v[96:97], v[104:105]
	v_pk_mul_f32 v[94:95], v[94:95], v[102:103]
	s_nop 0
	v_cvt_pk_bf16_f32 v94, v94, v95
	v_cvt_pk_bf16_f32 v95, v96, v97
	v_mov_b32_e32 v96, v184
	v_mov_b32_e32 v97, v185
	s_nop 0
	global_store_dwordx2 v[114:115], v[94:95], off offset:288
	s_nop 0
	v_lshlrev_b32_e32 v94, 16, v96
	v_and_b32_e32 v95, 0xffff0000, v96
	v_lshlrev_b32_e32 v96, 16, v97
	v_and_b32_e32 v97, 0xffff0000, v97
	v_pk_mul_f32 v[96:97], v[100:101], v[96:97]
	v_pk_mul_f32 v[94:95], v[98:99], v[94:95]
	v_lshlrev_b64 v[98:99], 12, v[106:107]
	v_cvt_pk_bf16_f32 v94, v94, v95
	v_cvt_pk_bf16_f32 v95, v96, v97
	v_mov_b32_e32 v96, v186
	v_mov_b32_e32 v97, v187
	v_lshl_add_u64 v[98:99], s[12:13], 0, v[98:99]
	v_lshl_add_u64 v[98:99], v[98:99], 0, v[142:143]
	global_store_dwordx2 v[98:99], v[94:95], off
	s_nop 0
	v_lshlrev_b32_e32 v94, 16, v96
	v_and_b32_e32 v95, 0xffff0000, v96
	v_lshlrev_b32_e32 v96, 16, v97
	v_and_b32_e32 v97, 0xffff0000, v97
	v_pk_mul_f32 v[92:93], v[92:93], v[96:97]
	v_pk_mul_f32 v[90:91], v[90:91], v[94:95]
	s_nop 0
	v_cvt_pk_bf16_f32 v90, v90, v91
	v_cvt_pk_bf16_f32 v91, v92, v93
	v_mov_b32_e32 v92, v188
	v_mov_b32_e32 v93, v189
	s_nop 0
	global_store_dwordx2 v[98:99], v[90:91], off offset:32
	s_nop 0
	v_lshlrev_b32_e32 v90, 16, v92
	v_and_b32_e32 v91, 0xffff0000, v92
	v_lshlrev_b32_e32 v92, 16, v93
	v_and_b32_e32 v93, 0xffff0000, v93
	v_pk_mul_f32 v[88:89], v[88:89], v[92:93]
	v_pk_mul_f32 v[86:87], v[86:87], v[90:91]
	v_or_b32_e32 v90, 48, v144
	v_cvt_pk_bf16_f32 v86, v86, v87
	v_cvt_pk_bf16_f32 v87, v88, v89
	v_mov_b32_e32 v88, v192
	v_mov_b32_e32 v89, v193
	v_mad_i64_i32 v[92:93], s[24:25], v90, s50, v[146:147]
	global_store_dwordx2 v[98:99], v[86:87], off offset:256
	v_lshl_add_u64 v[92:93], v[92:93], 0, v[142:143]
	v_ashrrev_i32_e32 v91, 31, v90
	s_nop 0
	v_lshlrev_b32_e32 v86, 16, v88
	v_and_b32_e32 v87, 0xffff0000, v88
	v_lshlrev_b32_e32 v88, 16, v89
	v_and_b32_e32 v89, 0xffff0000, v89
	v_pk_mul_f32 v[80:81], v[80:81], v[88:89]
	v_pk_mul_f32 v[78:79], v[78:79], v[86:87]
	s_nop 0
	v_cvt_pk_bf16_f32 v78, v78, v79
	v_cvt_pk_bf16_f32 v79, v80, v81
	v_mov_b32_e32 v80, v194
	v_mov_b32_e32 v81, v195
	s_nop 0
	global_store_dwordx2 v[98:99], v[78:79], off offset:288
	s_nop 0
	v_lshlrev_b32_e32 v78, 16, v80
	v_and_b32_e32 v79, 0xffff0000, v80
	v_lshlrev_b32_e32 v80, 16, v81
	v_and_b32_e32 v81, 0xffff0000, v81
	v_pk_mul_f32 v[80:81], v[84:85], v[80:81]
	v_pk_mul_f32 v[78:79], v[82:83], v[78:79]
	v_lshlrev_b64 v[82:83], 12, v[90:91]
	v_cvt_pk_bf16_f32 v78, v78, v79
	v_cvt_pk_bf16_f32 v79, v80, v81
	v_mov_b32_e32 v80, v196
	v_mov_b32_e32 v81, v197
	v_lshl_add_u64 v[82:83], s[12:13], 0, v[82:83]
	v_lshl_add_u64 v[82:83], v[82:83], 0, v[142:143]
	global_store_dwordx2 v[82:83], v[78:79], off
	s_nop 0
	v_lshlrev_b32_e32 v78, 16, v80
	v_and_b32_e32 v79, 0xffff0000, v80
	v_lshlrev_b32_e32 v80, 16, v81
	v_and_b32_e32 v81, 0xffff0000, v81
	v_pk_mul_f32 v[76:77], v[76:77], v[80:81]
	v_pk_mul_f32 v[74:75], v[74:75], v[78:79]
	s_nop 0
	v_cvt_pk_bf16_f32 v74, v74, v75
	v_cvt_pk_bf16_f32 v75, v76, v77
	v_mov_b32_e32 v76, v198
	v_mov_b32_e32 v77, v199
	s_nop 0
	global_store_dwordx2 v[82:83], v[74:75], off offset:32
	s_nop 0
	v_lshlrev_b32_e32 v74, 16, v76
	v_and_b32_e32 v75, 0xffff0000, v76
	v_lshlrev_b32_e32 v76, 16, v77
	v_and_b32_e32 v77, 0xffff0000, v77
	v_pk_mul_f32 v[72:73], v[72:73], v[76:77]
	v_pk_mul_f32 v[70:71], v[70:71], v[74:75]
	v_add_u32_e32 v74, 0x80, v144
	v_cvt_pk_bf16_f32 v70, v70, v71
	v_cvt_pk_bf16_f32 v71, v72, v73
	v_mov_b32_e32 v72, v200
	v_mov_b32_e32 v73, v201
	v_mad_i64_i32 v[76:77], s[24:25], v74, s50, v[146:147]
	global_store_dwordx2 v[82:83], v[70:71], off offset:256
	v_lshl_add_u64 v[76:77], v[76:77], 0, v[142:143]
	v_ashrrev_i32_e32 v75, 31, v74
	s_nop 0
	v_lshlrev_b32_e32 v70, 16, v72
	v_and_b32_e32 v71, 0xffff0000, v72
	v_lshlrev_b32_e32 v72, 16, v73
	v_and_b32_e32 v73, 0xffff0000, v73
	v_pk_mul_f32 v[68:69], v[68:69], v[72:73]
	v_pk_mul_f32 v[66:67], v[66:67], v[70:71]
	s_nop 0
	v_cvt_pk_bf16_f32 v66, v66, v67
	v_cvt_pk_bf16_f32 v67, v68, v69
	v_mov_b32_e32 v68, v202
	v_mov_b32_e32 v69, v203
	s_nop 0
	global_store_dwordx2 v[82:83], v[66:67], off offset:288
	s_nop 0
	v_lshlrev_b32_e32 v66, 16, v68
	v_and_b32_e32 v67, 0xffff0000, v68
	v_lshlrev_b32_e32 v68, 16, v69
	v_and_b32_e32 v69, 0xffff0000, v69
	v_pk_mul_f32 v[64:65], v[64:65], v[68:69]
	v_pk_mul_f32 v[62:63], v[62:63], v[66:67]
	v_lshlrev_b64 v[66:67], 12, v[74:75]
	v_cvt_pk_bf16_f32 v62, v62, v63
	v_cvt_pk_bf16_f32 v63, v64, v65
	v_mov_b32_e32 v64, v204
	v_mov_b32_e32 v65, v205
	v_lshl_add_u64 v[66:67], s[12:13], 0, v[66:67]
	v_lshl_add_u64 v[66:67], v[66:67], 0, v[142:143]
	global_store_dwordx2 v[66:67], v[62:63], off
	s_nop 0
	v_lshlrev_b32_e32 v62, 16, v64
	v_and_b32_e32 v63, 0xffff0000, v64
	v_lshlrev_b32_e32 v64, 16, v65
	v_and_b32_e32 v65, 0xffff0000, v65
	v_pk_mul_f32 v[60:61], v[60:61], v[64:65]
	v_pk_mul_f32 v[58:59], v[58:59], v[62:63]
	s_nop 0
	v_cvt_pk_bf16_f32 v58, v58, v59
	v_cvt_pk_bf16_f32 v59, v60, v61
	v_mov_b32_e32 v60, v206
	v_mov_b32_e32 v61, v207
	s_nop 0
	global_store_dwordx2 v[66:67], v[58:59], off offset:32
	s_nop 0
	v_lshlrev_b32_e32 v58, 16, v60
	v_and_b32_e32 v59, 0xffff0000, v60
	v_lshlrev_b32_e32 v60, 16, v61
	v_and_b32_e32 v61, 0xffff0000, v61
	v_pk_mul_f32 v[56:57], v[56:57], v[60:61]
	v_pk_mul_f32 v[54:55], v[54:55], v[58:59]
	v_add_u32_e32 v58, 0x90, v144
	v_cvt_pk_bf16_f32 v54, v54, v55
	v_cvt_pk_bf16_f32 v55, v56, v57
	v_mov_b32_e32 v56, v208
	v_mov_b32_e32 v57, v209
	v_mad_i64_i32 v[60:61], s[24:25], v58, s50, v[146:147]
	global_store_dwordx2 v[66:67], v[54:55], off offset:256
	v_lshl_add_u64 v[60:61], v[60:61], 0, v[142:143]
	v_ashrrev_i32_e32 v59, 31, v58
	s_nop 0
	v_lshlrev_b32_e32 v54, 16, v56
	v_and_b32_e32 v55, 0xffff0000, v56
	v_lshlrev_b32_e32 v56, 16, v57
	v_and_b32_e32 v57, 0xffff0000, v57
	v_pk_mul_f32 v[48:49], v[48:49], v[56:57]
	v_pk_mul_f32 v[46:47], v[46:47], v[54:55]
	s_nop 0
	v_cvt_pk_bf16_f32 v46, v46, v47
	v_cvt_pk_bf16_f32 v47, v48, v49
	v_mov_b32_e32 v48, v210
	v_mov_b32_e32 v49, v211
	s_nop 0
	global_store_dwordx2 v[66:67], v[46:47], off offset:288
	s_nop 0
	v_lshlrev_b32_e32 v46, 16, v48
	v_and_b32_e32 v47, 0xffff0000, v48
	v_lshlrev_b32_e32 v48, 16, v49
	v_and_b32_e32 v49, 0xffff0000, v49
	v_pk_mul_f32 v[48:49], v[52:53], v[48:49]
	v_pk_mul_f32 v[46:47], v[50:51], v[46:47]
	v_lshlrev_b64 v[50:51], 12, v[58:59]
	v_cvt_pk_bf16_f32 v46, v46, v47
	v_cvt_pk_bf16_f32 v47, v48, v49
	v_mov_b32_e32 v48, v212
	v_mov_b32_e32 v49, v213
	v_lshl_add_u64 v[50:51], s[12:13], 0, v[50:51]
	v_lshl_add_u64 v[50:51], v[50:51], 0, v[142:143]
	global_store_dwordx2 v[50:51], v[46:47], off
	s_nop 0
	v_lshlrev_b32_e32 v46, 16, v48
	v_and_b32_e32 v47, 0xffff0000, v48
	v_lshlrev_b32_e32 v48, 16, v49
	v_and_b32_e32 v49, 0xffff0000, v49
	v_pk_mul_f32 v[44:45], v[44:45], v[48:49]
	v_pk_mul_f32 v[42:43], v[42:43], v[46:47]
	s_nop 0
	v_cvt_pk_bf16_f32 v42, v42, v43
	v_cvt_pk_bf16_f32 v43, v44, v45
	v_mov_b32_e32 v44, v214
	v_mov_b32_e32 v45, v215
	s_nop 0
	global_store_dwordx2 v[50:51], v[42:43], off offset:32
	s_nop 0
	v_lshlrev_b32_e32 v42, 16, v44
	v_and_b32_e32 v43, 0xffff0000, v44
	v_lshlrev_b32_e32 v44, 16, v45
	v_and_b32_e32 v45, 0xffff0000, v45
	v_pk_mul_f32 v[40:41], v[40:41], v[44:45]
	v_pk_mul_f32 v[38:39], v[38:39], v[42:43]
	v_add_u32_e32 v42, 0xa0, v144
	v_cvt_pk_bf16_f32 v38, v38, v39
	v_cvt_pk_bf16_f32 v39, v40, v41
	v_mov_b32_e32 v40, v216
	v_mov_b32_e32 v41, v217
	v_mad_i64_i32 v[44:45], s[24:25], v42, s50, v[146:147]
	global_store_dwordx2 v[50:51], v[38:39], off offset:256
	v_lshl_add_u64 v[44:45], v[44:45], 0, v[142:143]
	v_ashrrev_i32_e32 v43, 31, v42
	s_nop 0
	v_lshlrev_b32_e32 v38, 16, v40
	v_and_b32_e32 v39, 0xffff0000, v40
	v_lshlrev_b32_e32 v40, 16, v41
	v_and_b32_e32 v41, 0xffff0000, v41
	v_pk_mul_f32 v[32:33], v[32:33], v[40:41]
	v_pk_mul_f32 v[30:31], v[30:31], v[38:39]
	s_nop 0
	v_cvt_pk_bf16_f32 v30, v30, v31
	v_cvt_pk_bf16_f32 v31, v32, v33
	v_mov_b32_e32 v32, v218
	v_mov_b32_e32 v33, v219
	s_nop 0
	global_store_dwordx2 v[50:51], v[30:31], off offset:288
	s_nop 0
	v_lshlrev_b32_e32 v30, 16, v32
	v_and_b32_e32 v31, 0xffff0000, v32
	v_lshlrev_b32_e32 v32, 16, v33
	v_and_b32_e32 v33, 0xffff0000, v33
	v_pk_mul_f32 v[32:33], v[36:37], v[32:33]
	v_pk_mul_f32 v[30:31], v[34:35], v[30:31]
	v_lshlrev_b64 v[34:35], 12, v[42:43]
	v_cvt_pk_bf16_f32 v30, v30, v31
	v_cvt_pk_bf16_f32 v31, v32, v33
	v_mov_b32_e32 v32, v220
	v_mov_b32_e32 v33, v221
	v_lshl_add_u64 v[34:35], s[12:13], 0, v[34:35]
	v_lshl_add_u64 v[34:35], v[34:35], 0, v[142:143]
	global_store_dwordx2 v[34:35], v[30:31], off
	s_nop 0
	v_lshlrev_b32_e32 v30, 16, v32
	v_and_b32_e32 v31, 0xffff0000, v32
	v_lshlrev_b32_e32 v32, 16, v33
	v_and_b32_e32 v33, 0xffff0000, v33
	v_pk_mul_f32 v[28:29], v[28:29], v[32:33]
	v_pk_mul_f32 v[26:27], v[26:27], v[30:31]
	s_nop 0
	v_cvt_pk_bf16_f32 v26, v26, v27
	v_cvt_pk_bf16_f32 v27, v28, v29
	v_mov_b32_e32 v28, v222
	v_mov_b32_e32 v29, v223
	s_nop 0
	global_store_dwordx2 v[34:35], v[26:27], off offset:32
	s_nop 0
	v_lshlrev_b32_e32 v26, 16, v28
	v_and_b32_e32 v27, 0xffff0000, v28
	v_lshlrev_b32_e32 v28, 16, v29
	v_and_b32_e32 v29, 0xffff0000, v29
	v_pk_mul_f32 v[24:25], v[24:25], v[28:29]
	v_pk_mul_f32 v[22:23], v[22:23], v[26:27]
	v_add_u32_e32 v26, 0xb0, v144
	v_cvt_pk_bf16_f32 v22, v22, v23
	v_cvt_pk_bf16_f32 v23, v24, v25
	v_mov_b32_e32 v24, v228
	v_mov_b32_e32 v25, v229
	v_mad_i64_i32 v[28:29], s[24:25], v26, s50, v[146:147]
	global_store_dwordx2 v[34:35], v[22:23], off offset:256
	v_lshl_add_u64 v[28:29], v[28:29], 0, v[142:143]
	v_ashrrev_i32_e32 v27, 31, v26
	s_mov_b64 s[24:25], s[18:19]
	s_nop 0
	v_lshlrev_b32_e32 v22, 16, v24
	v_and_b32_e32 v23, 0xffff0000, v24
	v_lshlrev_b32_e32 v24, 16, v25
	v_and_b32_e32 v25, 0xffff0000, v25
	v_pk_mul_f32 v[16:17], v[16:17], v[24:25]
	v_pk_mul_f32 v[14:15], v[14:15], v[22:23]
	s_nop 0
	v_cvt_pk_bf16_f32 v14, v14, v15
	v_cvt_pk_bf16_f32 v15, v16, v17
	v_mov_b32_e32 v16, v230
	v_mov_b32_e32 v17, v231
	s_nop 0
	global_store_dwordx2 v[34:35], v[14:15], off offset:288
	s_nop 0
	v_lshlrev_b32_e32 v14, 16, v16
	v_and_b32_e32 v15, 0xffff0000, v16
	v_lshlrev_b32_e32 v16, 16, v17
	v_and_b32_e32 v17, 0xffff0000, v17
	v_pk_mul_f32 v[16:17], v[20:21], v[16:17]
	v_pk_mul_f32 v[14:15], v[18:19], v[14:15]
	v_lshlrev_b64 v[18:19], 12, v[26:27]
	v_cvt_pk_bf16_f32 v14, v14, v15
	v_cvt_pk_bf16_f32 v15, v16, v17
	v_mov_b32_e32 v16, v232
	v_mov_b32_e32 v17, v233
	v_lshl_add_u64 v[18:19], s[12:13], 0, v[18:19]
	v_lshl_add_u64 v[18:19], v[18:19], 0, v[142:143]
	global_store_dwordx2 v[18:19], v[14:15], off
	s_nop 0
	v_lshlrev_b32_e32 v14, 16, v16
	v_and_b32_e32 v15, 0xffff0000, v16
	v_lshlrev_b32_e32 v16, 16, v17
	v_and_b32_e32 v17, 0xffff0000, v17
	v_pk_mul_f32 v[12:13], v[12:13], v[16:17]
	v_pk_mul_f32 v[10:11], v[10:11], v[14:15]
	s_nop 0
	v_cvt_pk_bf16_f32 v10, v10, v11
	v_cvt_pk_bf16_f32 v11, v12, v13
	v_mov_b32_e32 v12, v234
	v_mov_b32_e32 v13, v235
	s_nop 0
	global_store_dwordx2 v[18:19], v[10:11], off offset:32
	s_nop 0
	v_lshlrev_b32_e32 v10, 16, v12
	v_and_b32_e32 v11, 0xffff0000, v12
	v_lshlrev_b32_e32 v12, 16, v13
	v_and_b32_e32 v13, 0xffff0000, v13
	v_pk_mul_f32 v[8:9], v[8:9], v[12:13]
	v_pk_mul_f32 v[6:7], v[6:7], v[10:11]
	s_nop 0
	v_cvt_pk_bf16_f32 v6, v6, v7
	v_cvt_pk_bf16_f32 v7, v8, v9
	v_mov_b32_e32 v8, v236
	v_mov_b32_e32 v9, v237
	s_nop 0
	global_store_dwordx2 v[18:19], v[6:7], off offset:256
	s_nop 0
	v_lshlrev_b32_e32 v6, 16, v8
	v_and_b32_e32 v7, 0xffff0000, v8
	v_lshlrev_b32_e32 v8, 16, v9
	v_and_b32_e32 v9, 0xffff0000, v9
	v_pk_mul_f32 v[2:3], v[2:3], v[6:7]
	v_pk_mul_f32 v[4:5], v[4:5], v[8:9]
	v_cvt_pk_bf16_f32 v2, v2, v3
	s_nop 0
	v_cvt_pk_bf16_f32 v3, v4, v5
	global_store_dwordx2 v[18:19], v[2:3], off offset:288
	s_cbranch_vccz .LBB0_1196
	s_waitcnt vmcnt(0)
	s_cmp_lg_u32 s30, 0x100
	s_cbranch_scc1 .Ldt_p0
	s_cmp_lg_u32 s44, 3
	s_cbranch_scc1 .Ldt_p0
	buffer_wbl2 sc1
	s_waitcnt vmcnt(0)
	v_readlane_b32 s92, v250, 40
	v_readlane_b32 s93, v250, 41
	s_sub_i32 s94, s31, 0
	s_lshl_b32 s94, s94, 7
	s_add_i32 s94, s94, 0x10000
	s_add_u32 s92, s92, s94
	s_addc_u32 s93, s93, 0
	v_mov_b32_e32 v2, 0
	v_mov_b32_e32 v3, 1
	s_mov_b64 s[96:97], exec
	s_mov_b64 exec, 1
	global_atomic_add v2, v3, s[92:93]
	s_mov_b64 exec, s[96:97]
	s_waitcnt vmcnt(0)
.Ldt_p0:
	s_cmpk_gt_u32 s33, 0xff
	s_cbranch_scc1 .LBB0_1203
	s_barrier

.LBB0_1208:
	s_add_i32 s44, s44, 1
	s_mul_i32 s2, s44, s47
	s_mul_hi_u32 s3, s44, s30
	s_add_i32 s3, s3, s2
	s_mul_i32 s2, s44, s30
	s_add_u32 s18, s2, s31
	s_addc_u32 s19, s3, s39
	s_cmp_lg_u32 s30, 0x100
	s_cbranch_scc1 .Ldadj1
	s_cmp_lt_u32 s18, 0x200
	s_cbranch_scc1 .Ldadj1
	s_sub_i32 s18, s18, 8
	s_cmp_lt_u32 s18, 0x200
	s_cselect_b32 s18, 0x7fff, s18
.Ldadj1:
	v_cmp_gt_i64_e64 s[2:3], s[18:19], v[140:141]
	s_and_b64 vcc, exec, s[2:3]
	s_cbranch_vccnz .LBB0_1210
	s_ashr_i32 s14, s18, 31
	s_lshr_b32 s14, s14, 29
	s_add_i32 s14, s18, s14
	s_ashr_i32 s15, s14, 3
	s_and_b32 s14, s14, -8
	s_sub_i32 s14, s18, s14
	s_cmp_lt_i32 s14, 0
	s_cselect_b32 s16, s40, 0x41
	s_mul_i32 s14, s16, s14
	s_add_i32 s14, s14, s15
	s_ashr_i32 s15, s14, 31
	s_lshr_b32 s15, s15, 26
	s_add_i32 s15, s14, s15
	s_ashr_i32 s16, s15, 6
	s_lshl_b32 s16, s16, 3
	s_sub_i32 s17, 0x41, s16
	s_min_i32 s17, s17, 8
	s_abs_i32 s20, s17
	v_cvt_f32_u32_e32 v2, s20
	s_sub_i32 s28, 0, s20
	s_andn2_b32 s15, s15, 63
	s_sub_i32 s15, s14, s15
	v_rcp_iflag_f32_e32 v2, v2
	s_abs_i32 s14, s15
	s_xor_b32 s21, s15, s17
	s_ashr_i32 s21, s21, 31
	v_mul_f32_e32 v2, 0x4f7ffffe, v2
	v_cvt_u32_f32_e32 v2, v2
	s_nop 0
	v_readfirstlane_b32 s29, v2
	s_mul_i32 s28, s28, s29
	s_mul_hi_u32 s28, s29, s28
	s_add_i32 s29, s29, s28
	s_mul_hi_u32 s28, s14, s29
	s_mul_i32 s29, s28, s20
	s_sub_i32 s14, s14, s29
	s_add_i32 s53, s28, 1
	s_sub_i32 s29, s14, s20
	s_cmp_ge_u32 s14, s20
	s_cselect_b32 s28, s53, s28
	s_cselect_b32 s14, s29, s14
	s_add_i32 s29, s28, 1
	s_cmp_ge_u32 s14, s20
	s_cselect_b32 s14, s29, s28
	s_xor_b32 s14, s14, s21
	s_sub_i32 s14, s14, s21
	s_mul_i32 s17, s14, s17
	s_sub_i32 s15, s15, s17
	s_add_i32 s16, s15, s16

.LBB0_1211:
	ds_read_b128 v[142:145], v158
	ds_read_b128 v[162:165], v158 offset:1024
	ds_read_b128 v[166:169], v158 offset:2048
	ds_read_b128 v[170:173], v158 offset:3072
	s_add_u32 s26, s24, 0xfffc0080
	s_addc_u32 s27, s25, -1
	s_cmp_eq_u32 s57, 12
	s_cselect_b32 s29, s17, s27
	s_cselect_b32 s28, s53, s26
	s_cselect_b32 s27, s15, s56
	s_cselect_b32 s26, s54, s55
	v_lshl_add_u64 v[146:147], s[24:25], 0, v[134:135]
	s_add_i32 m0, s23, 0xc000
	ds_read_b128 v[174:177], v159
	ds_read_b128 v[178:181], v159 offset:1024
	ds_read_b128 v[182:185], v159 offset:2048
	ds_read_b128 v[186:189], v159 offset:3072
	ds_read_b128 v[192:195], v159 offset:4096
	ds_read_b128 v[196:199], v159 offset:5120
	ds_read_b128 v[200:203], v159 offset:6144
	ds_read_b128 v[204:207], v159 offset:7168
	global_load_lds_dwordx4 v[146:147], off
	v_lshl_add_u64 v[146:147], s[24:25], 0, v[136:137]
	s_add_i32 m0, s23, 0xe000
	s_nop 0
	global_load_lds_dwordx4 v[146:147], off
	s_waitcnt lgkmcnt(8)
	s_barrier
	s_waitcnt lgkmcnt(0)
	s_setprio 1
	s_waitcnt lgkmcnt(0)
	v_mfma_f32_16x16x32_bf16 v[126:129], v[142:145], v[174:177], v[126:129]
	v_mfma_f32_16x16x32_bf16 v[122:125], v[166:169], v[174:177], v[122:125]
	v_mfma_f32_16x16x32_bf16 v[110:113], v[142:145], v[182:185], v[110:113]
	v_mfma_f32_16x16x32_bf16 v[106:109], v[166:169], v[182:185], v[106:109]
	v_mfma_f32_16x16x32_bf16 v[94:97], v[142:145], v[192:195], v[94:97]
	v_mfma_f32_16x16x32_bf16 v[90:93], v[166:169], v[192:195], v[90:93]
	v_mfma_f32_16x16x32_bf16 v[78:81], v[142:145], v[200:203], v[78:81]
	v_mfma_f32_16x16x32_bf16 v[74:77], v[166:169], v[200:203], v[74:77]
	v_mfma_f32_16x16x32_bf16 v[126:129], v[162:165], v[178:181], v[126:129]
	v_mfma_f32_16x16x32_bf16 v[122:125], v[170:173], v[178:181], v[122:125]
	v_mfma_f32_16x16x32_bf16 v[110:113], v[162:165], v[186:189], v[110:113]
	v_mfma_f32_16x16x32_bf16 v[106:109], v[170:173], v[186:189], v[106:109]
	v_mfma_f32_16x16x32_bf16 v[94:97], v[162:165], v[196:199], v[94:97]
	v_mfma_f32_16x16x32_bf16 v[90:93], v[170:173], v[196:199], v[90:93]
	v_mfma_f32_16x16x32_bf16 v[78:81], v[162:165], v[204:207], v[78:81]
	v_mfma_f32_16x16x32_bf16 v[74:77], v[170:173], v[204:207], v[74:77]
	s_setprio 0
	s_barrier
	s_add_i32 s58, s48, s38
	v_lshl_add_u64 v[146:147], s[26:27], 0, v[130:131]
	s_mov_b32 m0, s58
	ds_read_b128 v[208:211], v160
	ds_read_b128 v[212:215], v160 offset:1024
	ds_read_b128 v[216:219], v160 offset:2048
	ds_read_b128 v[220:223], v160 offset:3072
	global_load_lds_dwordx4 v[146:147], off
	v_lshl_add_u64 v[190:191], s[26:27], 0, v[132:133]
	s_add_i32 m0, s58, 0x2000
	s_nop 0
	global_load_lds_dwordx4 v[190:191], off
	s_barrier
	s_waitcnt lgkmcnt(0)
	s_setprio 1
	s_waitcnt lgkmcnt(0)
	v_mfma_f32_16x16x32_bf16 v[118:121], v[208:211], v[174:177], v[118:121]
	v_mfma_f32_16x16x32_bf16 v[114:117], v[216:219], v[174:177], v[114:117]
	v_mfma_f32_16x16x32_bf16 v[102:105], v[208:211], v[182:185], v[102:105]
	v_mfma_f32_16x16x32_bf16 v[98:101], v[216:219], v[182:185], v[98:101]
	v_mfma_f32_16x16x32_bf16 v[86:89], v[208:211], v[192:195], v[86:89]
	v_mfma_f32_16x16x32_bf16 v[82:85], v[216:219], v[192:195], v[82:85]
	v_mfma_f32_16x16x32_bf16 v[70:73], v[208:211], v[200:203], v[70:73]
	v_mfma_f32_16x16x32_bf16 v[66:69], v[216:219], v[200:203], v[66:69]
	v_mfma_f32_16x16x32_bf16 v[118:121], v[212:215], v[178:181], v[118:121]
	v_mfma_f32_16x16x32_bf16 v[114:117], v[220:223], v[178:181], v[114:117]
	v_mfma_f32_16x16x32_bf16 v[102:105], v[212:215], v[186:189], v[102:105]
	v_mfma_f32_16x16x32_bf16 v[98:101], v[220:223], v[186:189], v[98:101]
	v_mfma_f32_16x16x32_bf16 v[86:89], v[212:215], v[196:199], v[86:89]
	v_mfma_f32_16x16x32_bf16 v[82:85], v[220:223], v[196:199], v[82:85]
	v_mfma_f32_16x16x32_bf16 v[70:73], v[212:215], v[204:207], v[70:73]
	v_mfma_f32_16x16x32_bf16 v[66:69], v[220:223], v[204:207], v[66:69]
	s_setprio 0
	s_mov_b32 m0, s23
	v_lshl_add_u64 v[224:225], s[28:29], 0, v[130:131]
	s_barrier
	ds_read_b128 v[174:177], v159 offset:16384
	ds_read_b128 v[178:181], v159 offset:17408
	ds_read_b128 v[182:185], v159 offset:18432
	ds_read_b128 v[186:189], v159 offset:19456
	ds_read_b128 v[192:195], v159 offset:20480
	ds_read_b128 v[196:199], v159 offset:21504
	ds_read_b128 v[200:203], v159 offset:22528
	ds_read_b128 v[204:207], v159 offset:23552
	global_load_lds_dwordx4 v[224:225], off
	v_lshl_add_u64 v[226:227], s[28:29], 0, v[132:133]
	s_mov_b32 m0, s41
	s_nop 0
	global_load_lds_dwordx4 v[226:227], off
	s_barrier
	s_waitcnt lgkmcnt(0)
	s_setprio 1
	s_waitcnt lgkmcnt(0)
	v_mfma_f32_16x16x32_bf16 v[62:65], v[142:145], v[174:177], v[62:65]
	v_mfma_f32_16x16x32_bf16 v[58:61], v[166:169], v[174:177], v[58:61]
	v_mfma_f32_16x16x32_bf16 v[46:49], v[142:145], v[182:185], v[46:49]
	v_mfma_f32_16x16x32_bf16 v[42:45], v[166:169], v[182:185], v[42:45]
	v_mfma_f32_16x16x32_bf16 v[30:33], v[142:145], v[192:195], v[30:33]
	v_mfma_f32_16x16x32_bf16 v[26:29], v[166:169], v[192:195], v[26:29]
	v_mfma_f32_16x16x32_bf16 v[14:17], v[142:145], v[200:203], v[14:17]
	v_mfma_f32_16x16x32_bf16 v[10:13], v[166:169], v[200:203], v[10:13]
	v_mfma_f32_16x16x32_bf16 v[62:65], v[162:165], v[178:181], v[62:65]
	v_mfma_f32_16x16x32_bf16 v[58:61], v[170:173], v[178:181], v[58:61]
	v_mfma_f32_16x16x32_bf16 v[46:49], v[162:165], v[186:189], v[46:49]
	v_mfma_f32_16x16x32_bf16 v[42:45], v[170:173], v[186:189], v[42:45]
	v_mfma_f32_16x16x32_bf16 v[30:33], v[162:165], v[196:199], v[30:33]
	v_mfma_f32_16x16x32_bf16 v[26:29], v[170:173], v[196:199], v[26:29]
	v_mfma_f32_16x16x32_bf16 v[14:17], v[162:165], v[204:207], v[14:17]
	v_mfma_f32_16x16x32_bf16 v[10:13], v[170:173], v[204:207], v[10:13]
	s_setprio 0
	s_barrier
	s_add_u32 s58, s26, 0x40000
	s_addc_u32 s59, s27, 0
	s_add_i32 s60, s49, s38
	v_lshl_add_u64 v[142:143], s[58:59], 0, v[130:131]
	s_mov_b32 m0, s60
	s_nop 0
	global_load_lds_dwordx4 v[142:143], off
	v_lshl_add_u64 v[142:143], s[58:59], 0, v[132:133]
	s_add_i32 m0, s60, 0x2000
	s_nop 0
	global_load_lds_dwordx4 v[142:143], off
	s_waitcnt vmcnt(6)
	s_barrier
	s_setprio 1
	v_mfma_f32_16x16x32_bf16 v[54:57], v[208:211], v[174:177], v[54:57]
	v_mfma_f32_16x16x32_bf16 v[50:53], v[216:219], v[174:177], v[50:53]
	v_mfma_f32_16x16x32_bf16 v[38:41], v[208:211], v[182:185], v[38:41]
	v_mfma_f32_16x16x32_bf16 v[34:37], v[216:219], v[182:185], v[34:37]
	v_mfma_f32_16x16x32_bf16 v[22:25], v[208:211], v[192:195], v[22:25]
	v_mfma_f32_16x16x32_bf16 v[18:21], v[216:219], v[192:195], v[18:21]
	v_mfma_f32_16x16x32_bf16 v[6:9], v[208:211], v[200:203], v[6:9]
	v_mfma_f32_16x16x32_bf16 v[2:5], v[216:219], v[200:203], v[2:5]
	v_mfma_f32_16x16x32_bf16 v[54:57], v[212:215], v[178:181], v[54:57]
	v_mfma_f32_16x16x32_bf16 v[50:53], v[220:223], v[178:181], v[50:53]
	v_mfma_f32_16x16x32_bf16 v[38:41], v[212:215], v[186:189], v[38:41]
	v_mfma_f32_16x16x32_bf16 v[34:37], v[220:223], v[186:189], v[34:37]
	v_mfma_f32_16x16x32_bf16 v[22:25], v[212:215], v[196:199], v[22:25]
	v_mfma_f32_16x16x32_bf16 v[18:21], v[220:223], v[196:199], v[18:21]
	v_mfma_f32_16x16x32_bf16 v[6:9], v[212:215], v[204:207], v[6:9]
	v_mfma_f32_16x16x32_bf16 v[2:5], v[220:223], v[204:207], v[2:5]
	s_setprio 0
	s_add_i32 s58, 0, 0x18000
	v_add_u32_e32 v161, s58, v156
	s_barrier
	ds_read_b128 v[142:145], v161
	ds_read_b128 v[162:165], v161 offset:1024
	ds_read_b128 v[166:169], v161 offset:2048
	ds_read_b128 v[170:173], v161 offset:3072
	s_add_u32 s28, s28, 0x40000
	s_addc_u32 s29, s29, 0
	s_mov_b32 m0, s42
	v_lshl_add_u64 v[208:209], s[28:29], 0, v[130:131]
	ds_read_b128 v[174:177], v159 offset:32768
	ds_read_b128 v[178:181], v159 offset:33792
	ds_read_b128 v[182:185], v159 offset:34816
	ds_read_b128 v[186:189], v159 offset:35840
	ds_read_b128 v[192:195], v159 offset:36864
	ds_read_b128 v[196:199], v159 offset:37888
	ds_read_b128 v[200:203], v159 offset:38912
	ds_read_b128 v[204:207], v159 offset:39936
	global_load_lds_dwordx4 v[208:209], off
	v_lshl_add_u64 v[208:209], s[28:29], 0, v[132:133]
	s_mov_b32 m0, s43
	s_nop 0
	global_load_lds_dwordx4 v[208:209], off
	s_waitcnt lgkmcnt(8)
	s_barrier
	s_waitcnt lgkmcnt(0)
	s_setprio 1
	s_waitcnt lgkmcnt(0)
	v_mfma_f32_16x16x32_bf16 v[126:129], v[142:145], v[174:177], v[126:129]
	v_mfma_f32_16x16x32_bf16 v[122:125], v[166:169], v[174:177], v[122:125]
	v_mfma_f32_16x16x32_bf16 v[110:113], v[142:145], v[182:185], v[110:113]
	v_mfma_f32_16x16x32_bf16 v[106:109], v[166:169], v[182:185], v[106:109]
	v_mfma_f32_16x16x32_bf16 v[94:97], v[142:145], v[192:195], v[94:97]
	v_mfma_f32_16x16x32_bf16 v[90:93], v[166:169], v[192:195], v[90:93]
	v_mfma_f32_16x16x32_bf16 v[78:81], v[142:145], v[200:203], v[78:81]
	v_mfma_f32_16x16x32_bf16 v[74:77], v[166:169], v[200:203], v[74:77]
	v_mfma_f32_16x16x32_bf16 v[126:129], v[162:165], v[178:181], v[126:129]
	v_mfma_f32_16x16x32_bf16 v[122:125], v[170:173], v[178:181], v[122:125]
	v_mfma_f32_16x16x32_bf16 v[110:113], v[162:165], v[186:189], v[110:113]
	v_mfma_f32_16x16x32_bf16 v[106:109], v[170:173], v[186:189], v[106:109]
	v_mfma_f32_16x16x32_bf16 v[94:97], v[162:165], v[196:199], v[94:97]
	v_mfma_f32_16x16x32_bf16 v[90:93], v[170:173], v[196:199], v[90:93]
	v_mfma_f32_16x16x32_bf16 v[78:81], v[162:165], v[204:207], v[78:81]
	v_mfma_f32_16x16x32_bf16 v[74:77], v[170:173], v[204:207], v[74:77]
	s_setprio 0
	s_barrier
	s_add_i32 s28, 0, 0x1c000
	s_add_i32 s29, s58, s38
	v_add_u32_e32 v161, s28, v156
	v_lshl_add_u64 v[146:147], v[146:147], 0, s[8:9]
	s_mov_b32 m0, s29
	ds_read_b128 v[208:211], v161
	ds_read_b128 v[212:215], v161 offset:1024
	ds_read_b128 v[216:219], v161 offset:2048
	ds_read_b128 v[220:223], v161 offset:3072
	global_load_lds_dwordx4 v[146:147], off
	v_lshl_add_u64 v[146:147], v[190:191], 0, s[8:9]
	s_add_i32 m0, s29, 0x2000
	s_nop 0
	global_load_lds_dwordx4 v[146:147], off
	s_barrier
	s_waitcnt lgkmcnt(0)
	s_setprio 1
	s_waitcnt lgkmcnt(0)
	v_mfma_f32_16x16x32_bf16 v[118:121], v[208:211], v[174:177], v[118:121]
	v_mfma_f32_16x16x32_bf16 v[114:117], v[216:219], v[174:177], v[114:117]
	v_mfma_f32_16x16x32_bf16 v[102:105], v[208:211], v[182:185], v[102:105]
	v_mfma_f32_16x16x32_bf16 v[98:101], v[216:219], v[182:185], v[98:101]
	v_mfma_f32_16x16x32_bf16 v[86:89], v[208:211], v[192:195], v[86:89]
	v_mfma_f32_16x16x32_bf16 v[82:85], v[216:219], v[192:195], v[82:85]
	v_mfma_f32_16x16x32_bf16 v[70:73], v[208:211], v[200:203], v[70:73]
	v_mfma_f32_16x16x32_bf16 v[66:69], v[216:219], v[200:203], v[66:69]
	v_mfma_f32_16x16x32_bf16 v[118:121], v[212:215], v[178:181], v[118:121]
	v_mfma_f32_16x16x32_bf16 v[114:117], v[220:223], v[178:181], v[114:117]
	v_mfma_f32_16x16x32_bf16 v[102:105], v[212:215], v[186:189], v[102:105]
	v_mfma_f32_16x16x32_bf16 v[98:101], v[220:223], v[186:189], v[98:101]
	v_mfma_f32_16x16x32_bf16 v[86:89], v[212:215], v[196:199], v[86:89]
	v_mfma_f32_16x16x32_bf16 v[82:85], v[220:223], v[196:199], v[82:85]
	v_mfma_f32_16x16x32_bf16 v[70:73], v[212:215], v[204:207], v[70:73]
	v_mfma_f32_16x16x32_bf16 v[66:69], v[220:223], v[204:207], v[66:69]
	s_setprio 0
	s_mov_b32 m0, s45
	v_lshl_add_u64 v[146:147], v[224:225], 0, s[8:9]
	s_barrier
	ds_read_b128 v[174:177], v159 offset:49152
	ds_read_b128 v[178:181], v159 offset:50176
	ds_read_b128 v[182:185], v159 offset:51200
	ds_read_b128 v[186:189], v159 offset:52224
	ds_read_b128 v[192:195], v159 offset:53248
	ds_read_b128 v[196:199], v159 offset:54272
	ds_read_b128 v[200:203], v159 offset:55296
	ds_read_b128 v[204:207], v159 offset:56320
	global_load_lds_dwordx4 v[146:147], off
	v_lshl_add_u64 v[146:147], v[226:227], 0, s[8:9]
	s_mov_b32 m0, s46
	s_nop 0
	global_load_lds_dwordx4 v[146:147], off
	s_barrier
	s_waitcnt lgkmcnt(0)
	s_setprio 1
	s_waitcnt lgkmcnt(0)
	v_mfma_f32_16x16x32_bf16 v[62:65], v[142:145], v[174:177], v[62:65]
	v_mfma_f32_16x16x32_bf16 v[58:61], v[166:169], v[174:177], v[58:61]
	v_mfma_f32_16x16x32_bf16 v[46:49], v[142:145], v[182:185], v[46:49]
	v_mfma_f32_16x16x32_bf16 v[42:45], v[166:169], v[182:185], v[42:45]
	v_mfma_f32_16x16x32_bf16 v[30:33], v[142:145], v[192:195], v[30:33]
	v_mfma_f32_16x16x32_bf16 v[26:29], v[166:169], v[192:195], v[26:29]
	v_mfma_f32_16x16x32_bf16 v[14:17], v[142:145], v[200:203], v[14:17]
	v_mfma_f32_16x16x32_bf16 v[10:13], v[166:169], v[200:203], v[10:13]
	v_mfma_f32_16x16x32_bf16 v[62:65], v[162:165], v[178:181], v[62:65]
	v_mfma_f32_16x16x32_bf16 v[58:61], v[170:173], v[178:181], v[58:61]
	v_mfma_f32_16x16x32_bf16 v[46:49], v[162:165], v[186:189], v[46:49]
	v_mfma_f32_16x16x32_bf16 v[42:45], v[170:173], v[186:189], v[42:45]
	v_mfma_f32_16x16x32_bf16 v[30:33], v[162:165], v[196:199], v[30:33]
	v_mfma_f32_16x16x32_bf16 v[26:29], v[170:173], v[196:199], v[26:29]
	v_mfma_f32_16x16x32_bf16 v[14:17], v[162:165], v[204:207], v[14:17]
	v_mfma_f32_16x16x32_bf16 v[10:13], v[170:173], v[204:207], v[10:13]
	s_setprio 0
	s_barrier
	s_add_u32 s26, s26, 0x40080
	s_addc_u32 s27, s27, 0
	s_add_i32 s28, s28, s38
	v_lshl_add_u64 v[142:143], s[26:27], 0, v[130:131]
	s_mov_b32 m0, s28
	s_nop 0
	global_load_lds_dwordx4 v[142:143], off
	v_lshl_add_u64 v[142:143], s[26:27], 0, v[132:133]
	s_add_i32 m0, s28, 0x2000
	s_nop 0
	global_load_lds_dwordx4 v[142:143], off
	s_waitcnt vmcnt(6)
	s_barrier
	s_setprio 1
	v_mfma_f32_16x16x32_bf16 v[54:57], v[208:211], v[174:177], v[54:57]
	v_mfma_f32_16x16x32_bf16 v[50:53], v[216:219], v[174:177], v[50:53]
	v_mfma_f32_16x16x32_bf16 v[38:41], v[208:211], v[182:185], v[38:41]
	v_mfma_f32_16x16x32_bf16 v[34:37], v[216:219], v[182:185], v[34:37]
	v_mfma_f32_16x16x32_bf16 v[22:25], v[208:211], v[192:195], v[22:25]
	v_mfma_f32_16x16x32_bf16 v[18:21], v[216:219], v[192:195], v[18:21]
	v_mfma_f32_16x16x32_bf16 v[6:9], v[208:211], v[200:203], v[6:9]
	v_mfma_f32_16x16x32_bf16 v[2:5], v[216:219], v[200:203], v[2:5]
	v_mfma_f32_16x16x32_bf16 v[54:57], v[212:215], v[178:181], v[54:57]
	v_mfma_f32_16x16x32_bf16 v[50:53], v[220:223], v[178:181], v[50:53]
	v_mfma_f32_16x16x32_bf16 v[38:41], v[212:215], v[186:189], v[38:41]
	v_mfma_f32_16x16x32_bf16 v[34:37], v[220:223], v[186:189], v[34:37]
	v_mfma_f32_16x16x32_bf16 v[22:25], v[212:215], v[196:199], v[22:25]
	v_mfma_f32_16x16x32_bf16 v[18:21], v[220:223], v[196:199], v[18:21]
	v_mfma_f32_16x16x32_bf16 v[6:9], v[212:215], v[204:207], v[6:9]
	v_mfma_f32_16x16x32_bf16 v[2:5], v[220:223], v[204:207], v[2:5]
	s_setprio 0
	s_add_i32 s57, s57, 2
	s_add_u32 s24, s24, 0x100
	s_addc_u32 s25, s25, 0
	s_add_u32 s55, s55, 0x100
	s_addc_u32 s56, s56, 0
	s_cmp_gt_u32 s57, 13
	s_barrier
	s_cbranch_scc0 .LBB0_1211
	s_cmp_lg_u32 s30, 0x100
	s_cbranch_scc1 .Ldt_c1
	s_cmp_lg_u32 s44, 3
	s_cbranch_scc1 .Ldt_c1
	v_readlane_b32 s92, v250, 40
	v_readlane_b32 s93, v250, 41
	s_sub_i32 s94, s31, 8
	s_lshl_b32 s94, s94, 7
	s_add_i32 s94, s94, 0x10000
	s_add_u32 s92, s92, s94
	s_addc_u32 s93, s93, 0
	s_mov_b32 s95, 0
	v_mov_b32_e32 v142, 0
.Ldt_c1_poll:
	global_load_dword v143, v142, s[92:93] sc1
	s_waitcnt vmcnt(0)
	v_readfirstlane_b32 s96, v143
	s_nop 3
	s_cmp_ge_u32 s96, 8
	s_cbranch_scc1 .Ldt_c1_got
	s_sleep 4
	s_add_i32 s95, s95, 1
	s_cmp_lt_u32 s95, 0x10000
	s_cbranch_scc1 .Ldt_c1_poll
.Ldt_c1_got:
	buffer_inv sc1
.Ldt_c1:
	v_lshl_or_b32 v142, s52, 8, v157
	v_lshl_add_u32 v144, s22, 8, v155
	v_ashrrev_i32_e32 v143, 31, v142
	v_mov_b64_e32 v[146:147], s[6:7]
	v_ashrrev_i32_e32 v145, 31, v144
	v_mad_i64_i32 v[162:163], s[24:25], v144, s50, v[146:147]
	v_lshlrev_b64 v[142:143], 1, v[142:143]
	v_lshl_add_u64 v[162:163], v[162:163], 0, v[142:143]
	v_lshlrev_b64 v[166:167], 12, v[144:145]
	v_add_co_u32_e32 v164, vcc, 0x2ec41000, v162
	v_lshl_add_u64 v[166:167], s[10:11], 0, v[166:167]
	s_nop 0
	v_addc_co_u32_e32 v165, vcc, 0, v163, vcc
	v_lshl_add_u64 v[166:167], v[166:167], 0, v[142:143]
	v_mov_b32_e32 v228, v164
	v_mov_b32_e32 v229, v165
	v_mov_b32_e32 v232, v166
	v_mov_b32_e32 v233, v167
	v_mov_b32_e32 v237, 0x1000
	global_load_dwordx2 v[174:175], v[228:229], off
	global_load_dwordx2 v[176:177], v[232:233], off
	global_load_dwordx2 v[178:179], v[228:229], off offset:32
	global_load_dwordx2 v[180:181], v[232:233], off offset:32
	global_load_dwordx2 v[182:183], v[228:229], off offset:256
	global_load_dwordx2 v[184:185], v[232:233], off offset:256
	global_load_dwordx2 v[186:187], v[228:229], off offset:288
	global_load_dwordx2 v[188:189], v[232:233], off offset:288
	v_mov_b32_e32 v236, 16
	v_mad_i64_i32 v[230:231], s[24:25], v236, s50, v[228:229]
	v_mad_i64_i32 v[234:235], s[24:25], v236, v237, v[232:233]
	global_load_dwordx2 v[192:193], v[230:231], off
	global_load_dwordx2 v[194:195], v[234:235], off
	global_load_dwordx2 v[196:197], v[230:231], off offset:32
	global_load_dwordx2 v[198:199], v[234:235], off offset:32
	global_load_dwordx2 v[200:201], v[230:231], off offset:256
	global_load_dwordx2 v[202:203], v[234:235], off offset:256
	global_load_dwordx2 v[204:205], v[230:231], off offset:288
	global_load_dwordx2 v[206:207], v[234:235], off offset:288
	v_mov_b32_e32 v236, 32
	v_mad_i64_i32 v[230:231], s[24:25], v236, s50, v[228:229]
	v_mad_i64_i32 v[234:235], s[24:25], v236, v237, v[232:233]
	global_load_dwordx2 v[208:209], v[230:231], off
	global_load_dwordx2 v[210:211], v[234:235], off
	global_load_dwordx2 v[212:213], v[230:231], off offset:32
	global_load_dwordx2 v[214:215], v[234:235], off offset:32
	global_load_dwordx2 v[216:217], v[230:231], off offset:256
	global_load_dwordx2 v[218:219], v[234:235], off offset:256
	global_load_dwordx2 v[220:221], v[230:231], off offset:288
	global_load_dwordx2 v[222:223], v[234:235], off offset:288
	s_waitcnt vmcnt(0)
	v_mov_b32_e32 v164, v174
	v_mov_b32_e32 v165, v175
	v_lshl_add_u64 v[162:163], v[162:163], 0, s[12:13]
	v_mov_b32_e32 v168, v176
	v_mov_b32_e32 v169, v177
	s_mov_b32 s52, s14
	s_mov_b32 s22, s16
	s_mov_b64 s[26:27], s[20:21]
	s_nop 0
	v_lshlrev_b32_e32 v170, 16, v164
	v_and_b32_e32 v171, 0xffff0000, v164
	v_lshlrev_b32_e32 v164, 16, v165
	v_and_b32_e32 v165, 0xffff0000, v165
	v_lshlrev_b32_e32 v172, 16, v168
	v_and_b32_e32 v173, 0xffff0000, v168
	v_lshlrev_b32_e32 v168, 16, v169
	v_and_b32_e32 v169, 0xffff0000, v169
	v_pk_fma_f32 v[128:129], v[128:129], v[164:165], v[168:169]
	v_pk_fma_f32 v[126:127], v[126:127], v[170:171], v[172:173]
	s_nop 0
	v_cvt_pk_bf16_f32 v126, v126, v127
	v_cvt_pk_bf16_f32 v127, v128, v129
	v_mov_b32_e32 v128, v178
	v_mov_b32_e32 v129, v179
	v_mov_b32_e32 v164, v180
	v_mov_b32_e32 v165, v181
	s_nop 0
	v_lshlrev_b32_e32 v168, 16, v164
	global_store_dwordx2 v[166:167], v[126:127], off
	v_lshlrev_b32_e32 v126, 16, v128
	v_and_b32_e32 v127, 0xffff0000, v128
	v_lshlrev_b32_e32 v128, 16, v129
	v_and_b32_e32 v129, 0xffff0000, v129
	v_and_b32_e32 v169, 0xffff0000, v164
	v_lshlrev_b32_e32 v164, 16, v165
	v_and_b32_e32 v165, 0xffff0000, v165
	v_pk_fma_f32 v[124:125], v[124:125], v[128:129], v[164:165]
	v_pk_fma_f32 v[122:123], v[122:123], v[126:127], v[168:169]
	s_nop 0
	v_cvt_pk_bf16_f32 v122, v122, v123
	v_cvt_pk_bf16_f32 v123, v124, v125
	v_mov_b32_e32 v124, v182
	v_mov_b32_e32 v125, v183
	v_mov_b32_e32 v126, v184
	v_mov_b32_e32 v127, v185
	s_nop 0
	v_lshlrev_b32_e32 v128, 16, v126
	global_store_dwordx2 v[166:167], v[122:123], off offset:32
	v_lshlrev_b32_e32 v122, 16, v124
	v_and_b32_e32 v123, 0xffff0000, v124
	v_lshlrev_b32_e32 v124, 16, v125
	v_and_b32_e32 v125, 0xffff0000, v125
	v_and_b32_e32 v129, 0xffff0000, v126
	v_lshlrev_b32_e32 v126, 16, v127
	v_and_b32_e32 v127, 0xffff0000, v127
	v_pk_fma_f32 v[120:121], v[120:121], v[124:125], v[126:127]
	v_pk_fma_f32 v[118:119], v[118:119], v[122:123], v[128:129]
	v_or_b32_e32 v124, 16, v144
	v_cvt_pk_bf16_f32 v118, v118, v119
	v_cvt_pk_bf16_f32 v119, v120, v121
	v_mov_b32_e32 v120, v186
	v_mov_b32_e32 v121, v187
	v_mov_b32_e32 v122, v188
	v_mov_b32_e32 v123, v189
	v_ashrrev_i32_e32 v125, 31, v124
	v_mad_i64_i32 v[126:127], s[24:25], v124, s50, v[146:147]
	global_store_dwordx2 v[166:167], v[118:119], off offset:256
	v_lshl_add_u64 v[126:127], v[126:127], 0, v[142:143]
	v_add_co_u32_e32 v128, vcc, s51, v126
	s_nop 0
	v_lshlrev_b32_e32 v118, 16, v120
	v_and_b32_e32 v119, 0xffff0000, v120
	v_lshlrev_b32_e32 v162, 16, v122
	v_and_b32_e32 v163, 0xffff0000, v122
	v_pk_fma_f32 v[114:115], v[114:115], v[118:119], v[162:163]
	v_lshlrev_b64 v[118:119], 12, v[124:125]
	v_lshlrev_b32_e32 v120, 16, v121
	v_and_b32_e32 v121, 0xffff0000, v121
	v_lshlrev_b32_e32 v122, 16, v123
	v_and_b32_e32 v123, 0xffff0000, v123
	v_lshl_add_u64 v[118:119], s[10:11], 0, v[118:119]
	v_addc_co_u32_e32 v129, vcc, 0, v127, vcc
	v_pk_fma_f32 v[116:117], v[116:117], v[120:121], v[122:123]
	v_lshl_add_u64 v[118:119], v[118:119], 0, v[142:143]
	v_cvt_pk_bf16_f32 v114, v114, v115
	v_cvt_pk_bf16_f32 v115, v116, v117
	v_mov_b32_e32 v116, v192
	v_mov_b32_e32 v117, v193
	v_mov_b32_e32 v120, v194
	v_mov_b32_e32 v121, v195
	v_lshl_add_u64 v[122:123], v[126:127], 0, s[12:13]
	global_store_dwordx2 v[166:167], v[114:115], off offset:288
	s_nop 0
	v_lshlrev_b32_e32 v114, 16, v116
	v_and_b32_e32 v115, 0xffff0000, v116
	v_lshlrev_b32_e32 v116, 16, v117
	v_and_b32_e32 v117, 0xffff0000, v117
	v_lshlrev_b32_e32 v124, 16, v120
	v_and_b32_e32 v125, 0xffff0000, v120
	v_lshlrev_b32_e32 v120, 16, v121
	v_and_b32_e32 v121, 0xffff0000, v121
	v_pk_fma_f32 v[112:113], v[112:113], v[116:117], v[120:121]
	v_pk_fma_f32 v[110:111], v[110:111], v[114:115], v[124:125]
	s_nop 0
	v_cvt_pk_bf16_f32 v110, v110, v111
	v_cvt_pk_bf16_f32 v111, v112, v113
	v_mov_b32_e32 v112, v196
	v_mov_b32_e32 v113, v197
	v_mov_b32_e32 v114, v198
	v_mov_b32_e32 v115, v199
	s_nop 0
	v_lshlrev_b32_e32 v116, 16, v114
	global_store_dwordx2 v[118:119], v[110:111], off
	v_lshlrev_b32_e32 v110, 16, v112
	v_and_b32_e32 v111, 0xffff0000, v112
	v_lshlrev_b32_e32 v112, 16, v113
	v_and_b32_e32 v113, 0xffff0000, v113
	v_and_b32_e32 v117, 0xffff0000, v114
	v_lshlrev_b32_e32 v114, 16, v115
	v_and_b32_e32 v115, 0xffff0000, v115
	v_pk_fma_f32 v[108:109], v[108:109], v[112:113], v[114:115]
	v_pk_fma_f32 v[106:107], v[106:107], v[110:111], v[116:117]
	s_nop 0
	v_cvt_pk_bf16_f32 v106, v106, v107
	v_cvt_pk_bf16_f32 v107, v108, v109
	v_mov_b32_e32 v108, v200
	v_mov_b32_e32 v109, v201
	v_mov_b32_e32 v110, v202
	v_mov_b32_e32 v111, v203
	s_nop 0
	v_lshlrev_b32_e32 v112, 16, v110
	global_store_dwordx2 v[118:119], v[106:107], off offset:32
	v_lshlrev_b32_e32 v106, 16, v108
	v_and_b32_e32 v107, 0xffff0000, v108
	v_lshlrev_b32_e32 v108, 16, v109
	v_and_b32_e32 v109, 0xffff0000, v109
	v_and_b32_e32 v113, 0xffff0000, v110
	v_lshlrev_b32_e32 v110, 16, v111
	v_and_b32_e32 v111, 0xffff0000, v111
	v_pk_fma_f32 v[104:105], v[104:105], v[108:109], v[110:111]
	v_pk_fma_f32 v[102:103], v[102:103], v[106:107], v[112:113]
	v_or_b32_e32 v108, 32, v144
	v_cvt_pk_bf16_f32 v102, v102, v103
	v_cvt_pk_bf16_f32 v103, v104, v105
	v_mov_b32_e32 v104, v204
	v_mov_b32_e32 v105, v205
	v_mov_b32_e32 v106, v206
	v_mov_b32_e32 v107, v207
	v_ashrrev_i32_e32 v109, 31, v108
	v_mad_i64_i32 v[110:111], s[24:25], v108, s50, v[146:147]
	global_store_dwordx2 v[118:119], v[102:103], off offset:256
	v_lshl_add_u64 v[110:111], v[110:111], 0, v[142:143]
	v_add_co_u32_e32 v112, vcc, s51, v110
	s_nop 0
	v_lshlrev_b32_e32 v102, 16, v104
	v_and_b32_e32 v103, 0xffff0000, v104
	v_lshlrev_b32_e32 v114, 16, v106
	v_and_b32_e32 v115, 0xffff0000, v106
	v_pk_fma_f32 v[98:99], v[98:99], v[102:103], v[114:115]
	v_lshlrev_b64 v[102:103], 12, v[108:109]
	v_lshlrev_b32_e32 v104, 16, v105
	v_and_b32_e32 v105, 0xffff0000, v105
	v_lshlrev_b32_e32 v106, 16, v107
	v_and_b32_e32 v107, 0xffff0000, v107
	v_lshl_add_u64 v[102:103], s[10:11], 0, v[102:103]
	v_addc_co_u32_e32 v113, vcc, 0, v111, vcc
	v_pk_fma_f32 v[100:101], v[100:101], v[104:105], v[106:107]
	v_lshl_add_u64 v[102:103], v[102:103], 0, v[142:143]
	v_cvt_pk_bf16_f32 v98, v98, v99
	v_cvt_pk_bf16_f32 v99, v100, v101
	v_mov_b32_e32 v100, v208
	v_mov_b32_e32 v101, v209
	v_mov_b32_e32 v104, v210
	v_mov_b32_e32 v105, v211
	v_lshl_add_u64 v[106:107], v[110:111], 0, s[12:13]
	global_store_dwordx2 v[118:119], v[98:99], off offset:288
	s_nop 0
	v_lshlrev_b32_e32 v98, 16, v100
	v_and_b32_e32 v99, 0xffff0000, v100
	v_lshlrev_b32_e32 v100, 16, v101
	v_and_b32_e32 v101, 0xffff0000, v101
	v_lshlrev_b32_e32 v108, 16, v104
	v_and_b32_e32 v109, 0xffff0000, v104
	v_lshlrev_b32_e32 v104, 16, v105
	v_and_b32_e32 v105, 0xffff0000, v105
	v_pk_fma_f32 v[96:97], v[96:97], v[100:101], v[104:105]
	v_pk_fma_f32 v[94:95], v[94:95], v[98:99], v[108:109]
	s_nop 0
	v_cvt_pk_bf16_f32 v94, v94, v95
	v_cvt_pk_bf16_f32 v95, v96, v97
	v_mov_b32_e32 v96, v212
	v_mov_b32_e32 v97, v213
	v_mov_b32_e32 v98, v214
	v_mov_b32_e32 v99, v215
	s_nop 0
	v_lshlrev_b32_e32 v100, 16, v98
	global_store_dwordx2 v[102:103], v[94:95], off
	v_lshlrev_b32_e32 v94, 16, v96
	v_and_b32_e32 v95, 0xffff0000, v96
	v_lshlrev_b32_e32 v96, 16, v97
	v_and_b32_e32 v97, 0xffff0000, v97
	v_and_b32_e32 v101, 0xffff0000, v98
	v_lshlrev_b32_e32 v98, 16, v99
	v_and_b32_e32 v99, 0xffff0000, v99
	v_pk_fma_f32 v[92:93], v[92:93], v[96:97], v[98:99]
	v_pk_fma_f32 v[90:91], v[90:91], v[94:95], v[100:101]
	s_nop 0
	v_cvt_pk_bf16_f32 v90, v90, v91
	v_cvt_pk_bf16_f32 v91, v92, v93
	v_mov_b32_e32 v92, v216
	v_mov_b32_e32 v93, v217
	v_mov_b32_e32 v94, v218
	v_mov_b32_e32 v95, v219
	s_nop 0
	v_lshlrev_b32_e32 v96, 16, v94
	global_store_dwordx2 v[102:103], v[90:91], off offset:32
	v_lshlrev_b32_e32 v90, 16, v92
	v_and_b32_e32 v91, 0xffff0000, v92
	v_lshlrev_b32_e32 v92, 16, v93
	v_and_b32_e32 v93, 0xffff0000, v93
	v_and_b32_e32 v97, 0xffff0000, v94
	v_lshlrev_b32_e32 v94, 16, v95
	v_and_b32_e32 v95, 0xffff0000, v95
	v_pk_fma_f32 v[88:89], v[88:89], v[92:93], v[94:95]
	v_pk_fma_f32 v[86:87], v[86:87], v[90:91], v[96:97]
	v_or_b32_e32 v92, 48, v144
	v_cvt_pk_bf16_f32 v86, v86, v87
	v_cvt_pk_bf16_f32 v87, v88, v89
	v_mov_b32_e32 v88, v220
	v_mov_b32_e32 v89, v221
	v_mov_b32_e32 v90, v222
	v_mov_b32_e32 v91, v223
	v_ashrrev_i32_e32 v93, 31, v92
	v_mad_i64_i32 v[94:95], s[24:25], v92, s50, v[146:147]
	global_store_dwordx2 v[102:103], v[86:87], off offset:256
	v_lshl_add_u64 v[94:95], v[94:95], 0, v[142:143]
	v_add_co_u32_e32 v96, vcc, s51, v94
	s_nop 0
	v_lshlrev_b32_e32 v86, 16, v88
	v_and_b32_e32 v87, 0xffff0000, v88
	v_lshlrev_b32_e32 v98, 16, v90
	v_and_b32_e32 v99, 0xffff0000, v90
	v_pk_fma_f32 v[82:83], v[82:83], v[86:87], v[98:99]
	v_lshlrev_b64 v[86:87], 12, v[92:93]
	v_lshlrev_b32_e32 v88, 16, v89
	v_and_b32_e32 v89, 0xffff0000, v89
	v_lshlrev_b32_e32 v90, 16, v91
	v_and_b32_e32 v91, 0xffff0000, v91
	v_lshl_add_u64 v[86:87], s[10:11], 0, v[86:87]
	v_addc_co_u32_e32 v97, vcc, 0, v95, vcc
	v_pk_fma_f32 v[84:85], v[84:85], v[88:89], v[90:91]
	v_lshl_add_u64 v[86:87], v[86:87], 0, v[142:143]
	v_cvt_pk_bf16_f32 v82, v82, v83
	v_cvt_pk_bf16_f32 v83, v84, v85
	v_mov_b32_e32 v237, 0x1000
	v_mov_b32_e32 v236, 48
	v_mad_i64_i32 v[230:231], s[24:25], v236, s50, v[228:229]
	v_mad_i64_i32 v[234:235], s[24:25], v236, v237, v[232:233]
	global_load_dwordx2 v[174:175], v[230:231], off
	global_load_dwordx2 v[176:177], v[234:235], off
	global_load_dwordx2 v[178:179], v[230:231], off offset:32
	global_load_dwordx2 v[180:181], v[234:235], off offset:32
	global_load_dwordx2 v[182:183], v[230:231], off offset:256
	global_load_dwordx2 v[184:185], v[234:235], off offset:256
	global_load_dwordx2 v[186:187], v[230:231], off offset:288
	global_load_dwordx2 v[188:189], v[234:235], off offset:288
	v_mov_b32_e32 v236, 128
	v_mad_i64_i32 v[230:231], s[24:25], v236, s50, v[228:229]
	v_mad_i64_i32 v[234:235], s[24:25], v236, v237, v[232:233]
	global_load_dwordx2 v[192:193], v[230:231], off
	global_load_dwordx2 v[194:195], v[234:235], off
	global_load_dwordx2 v[196:197], v[230:231], off offset:32
	global_load_dwordx2 v[198:199], v[234:235], off offset:32
	global_load_dwordx2 v[200:201], v[230:231], off offset:256
	global_load_dwordx2 v[202:203], v[234:235], off offset:256
	global_load_dwordx2 v[204:205], v[230:231], off offset:288
	global_load_dwordx2 v[206:207], v[234:235], off offset:288
	v_mov_b32_e32 v236, 144
	v_mad_i64_i32 v[230:231], s[24:25], v236, s50, v[228:229]
	v_mad_i64_i32 v[234:235], s[24:25], v236, v237, v[232:233]
	global_load_dwordx2 v[208:209], v[230:231], off
	global_load_dwordx2 v[210:211], v[234:235], off
	global_load_dwordx2 v[212:213], v[230:231], off offset:32
	global_load_dwordx2 v[214:215], v[234:235], off offset:32
	global_load_dwordx2 v[216:217], v[230:231], off offset:256
	global_load_dwordx2 v[218:219], v[234:235], off offset:256
	global_load_dwordx2 v[220:221], v[230:231], off offset:288
	global_load_dwordx2 v[222:223], v[234:235], off offset:288
	s_waitcnt vmcnt(0)
	v_mov_b32_e32 v84, v174
	v_mov_b32_e32 v85, v175
	v_mov_b32_e32 v88, v176
	v_mov_b32_e32 v89, v177
	v_lshl_add_u64 v[90:91], v[94:95], 0, s[12:13]
	global_store_dwordx2 v[102:103], v[82:83], off offset:288
	s_nop 0
	v_lshlrev_b32_e32 v82, 16, v84
	v_and_b32_e32 v83, 0xffff0000, v84
	v_lshlrev_b32_e32 v84, 16, v85
	v_and_b32_e32 v85, 0xffff0000, v85
	v_lshlrev_b32_e32 v92, 16, v88
	v_and_b32_e32 v93, 0xffff0000, v88
	v_lshlrev_b32_e32 v88, 16, v89
	v_and_b32_e32 v89, 0xffff0000, v89
	v_pk_fma_f32 v[80:81], v[80:81], v[84:85], v[88:89]
	v_pk_fma_f32 v[78:79], v[78:79], v[82:83], v[92:93]
	s_nop 0
	v_cvt_pk_bf16_f32 v78, v78, v79
	v_cvt_pk_bf16_f32 v79, v80, v81
	v_mov_b32_e32 v80, v178
	v_mov_b32_e32 v81, v179
	v_mov_b32_e32 v82, v180
	v_mov_b32_e32 v83, v181
	s_nop 0
	v_lshlrev_b32_e32 v84, 16, v82
	global_store_dwordx2 v[86:87], v[78:79], off
	v_lshlrev_b32_e32 v78, 16, v80
	v_and_b32_e32 v79, 0xffff0000, v80
	v_lshlrev_b32_e32 v80, 16, v81
	v_and_b32_e32 v81, 0xffff0000, v81
	v_and_b32_e32 v85, 0xffff0000, v82
	v_lshlrev_b32_e32 v82, 16, v83
	v_and_b32_e32 v83, 0xffff0000, v83
	v_pk_fma_f32 v[76:77], v[76:77], v[80:81], v[82:83]
	v_pk_fma_f32 v[74:75], v[74:75], v[78:79], v[84:85]
	s_nop 0
	v_cvt_pk_bf16_f32 v74, v74, v75
	v_cvt_pk_bf16_f32 v75, v76, v77
	v_mov_b32_e32 v76, v182
	v_mov_b32_e32 v77, v183
	v_mov_b32_e32 v78, v184
	v_mov_b32_e32 v79, v185
	s_nop 0
	v_lshlrev_b32_e32 v80, 16, v78
	global_store_dwordx2 v[86:87], v[74:75], off offset:32
	v_lshlrev_b32_e32 v74, 16, v76
	v_and_b32_e32 v75, 0xffff0000, v76
	v_lshlrev_b32_e32 v76, 16, v77
	v_and_b32_e32 v77, 0xffff0000, v77
	v_and_b32_e32 v81, 0xffff0000, v78
	v_lshlrev_b32_e32 v78, 16, v79
	v_and_b32_e32 v79, 0xffff0000, v79
	v_pk_fma_f32 v[72:73], v[72:73], v[76:77], v[78:79]
	v_pk_fma_f32 v[70:71], v[70:71], v[74:75], v[80:81]
	v_add_u32_e32 v76, 0x80, v144
	v_cvt_pk_bf16_f32 v70, v70, v71
	v_cvt_pk_bf16_f32 v71, v72, v73
	v_mov_b32_e32 v72, v186
	v_mov_b32_e32 v73, v187
	v_mov_b32_e32 v74, v188
	v_mov_b32_e32 v75, v189
	v_ashrrev_i32_e32 v77, 31, v76
	v_mad_i64_i32 v[78:79], s[24:25], v76, s50, v[146:147]
	global_store_dwordx2 v[86:87], v[70:71], off offset:256
	v_lshl_add_u64 v[78:79], v[78:79], 0, v[142:143]
	v_add_co_u32_e32 v80, vcc, s51, v78
	s_nop 0
	v_lshlrev_b32_e32 v70, 16, v72
	v_and_b32_e32 v71, 0xffff0000, v72
	v_lshlrev_b32_e32 v82, 16, v74
	v_and_b32_e32 v83, 0xffff0000, v74
	v_pk_fma_f32 v[66:67], v[66:67], v[70:71], v[82:83]
	v_lshlrev_b64 v[70:71], 12, v[76:77]
	v_lshlrev_b32_e32 v72, 16, v73
	v_and_b32_e32 v73, 0xffff0000, v73
	v_lshlrev_b32_e32 v74, 16, v75
	v_and_b32_e32 v75, 0xffff0000, v75
	v_lshl_add_u64 v[70:71], s[10:11], 0, v[70:71]
	v_addc_co_u32_e32 v81, vcc, 0, v79, vcc
	v_pk_fma_f32 v[68:69], v[68:69], v[72:73], v[74:75]
	v_lshl_add_u64 v[70:71], v[70:71], 0, v[142:143]
	v_cvt_pk_bf16_f32 v66, v66, v67
	v_cvt_pk_bf16_f32 v67, v68, v69
	v_mov_b32_e32 v68, v192
	v_mov_b32_e32 v69, v193
	v_mov_b32_e32 v72, v194
	v_mov_b32_e32 v73, v195
	v_lshl_add_u64 v[74:75], v[78:79], 0, s[12:13]
	global_store_dwordx2 v[86:87], v[66:67], off offset:288
	s_nop 0
	v_lshlrev_b32_e32 v66, 16, v68
	v_and_b32_e32 v67, 0xffff0000, v68
	v_lshlrev_b32_e32 v68, 16, v69
	v_and_b32_e32 v69, 0xffff0000, v69
	v_lshlrev_b32_e32 v76, 16, v72
	v_and_b32_e32 v77, 0xffff0000, v72
	v_lshlrev_b32_e32 v72, 16, v73
	v_and_b32_e32 v73, 0xffff0000, v73
	v_pk_fma_f32 v[64:65], v[64:65], v[68:69], v[72:73]
	v_pk_fma_f32 v[62:63], v[62:63], v[66:67], v[76:77]
	s_nop 0
	v_cvt_pk_bf16_f32 v62, v62, v63
	v_cvt_pk_bf16_f32 v63, v64, v65
	v_mov_b32_e32 v64, v196
	v_mov_b32_e32 v65, v197
	v_mov_b32_e32 v66, v198
	v_mov_b32_e32 v67, v199
	s_nop 0
	v_lshlrev_b32_e32 v68, 16, v66
	global_store_dwordx2 v[70:71], v[62:63], off
	v_lshlrev_b32_e32 v62, 16, v64
	v_and_b32_e32 v63, 0xffff0000, v64
	v_lshlrev_b32_e32 v64, 16, v65
	v_and_b32_e32 v65, 0xffff0000, v65
	v_and_b32_e32 v69, 0xffff0000, v66
	v_lshlrev_b32_e32 v66, 16, v67
	v_and_b32_e32 v67, 0xffff0000, v67
	v_pk_fma_f32 v[60:61], v[60:61], v[64:65], v[66:67]
	v_pk_fma_f32 v[58:59], v[58:59], v[62:63], v[68:69]
	s_nop 0
	v_cvt_pk_bf16_f32 v58, v58, v59
	v_cvt_pk_bf16_f32 v59, v60, v61
	v_mov_b32_e32 v60, v200
	v_mov_b32_e32 v61, v201
	v_mov_b32_e32 v62, v202
	v_mov_b32_e32 v63, v203
	s_nop 0
	v_lshlrev_b32_e32 v64, 16, v62
	global_store_dwordx2 v[70:71], v[58:59], off offset:32
	v_lshlrev_b32_e32 v58, 16, v60
	v_and_b32_e32 v59, 0xffff0000, v60
	v_lshlrev_b32_e32 v60, 16, v61
	v_and_b32_e32 v61, 0xffff0000, v61
	v_and_b32_e32 v65, 0xffff0000, v62
	v_lshlrev_b32_e32 v62, 16, v63
	v_and_b32_e32 v63, 0xffff0000, v63
	v_pk_fma_f32 v[56:57], v[56:57], v[60:61], v[62:63]
	v_pk_fma_f32 v[54:55], v[54:55], v[58:59], v[64:65]
	v_add_u32_e32 v60, 0x90, v144
	v_cvt_pk_bf16_f32 v54, v54, v55
	v_cvt_pk_bf16_f32 v55, v56, v57
	v_mov_b32_e32 v56, v204
	v_mov_b32_e32 v57, v205
	v_mov_b32_e32 v58, v206
	v_mov_b32_e32 v59, v207
	v_ashrrev_i32_e32 v61, 31, v60
	v_mad_i64_i32 v[62:63], s[24:25], v60, s50, v[146:147]
	global_store_dwordx2 v[70:71], v[54:55], off offset:256
	v_lshl_add_u64 v[62:63], v[62:63], 0, v[142:143]
	v_add_co_u32_e32 v64, vcc, s51, v62
	s_nop 0
	v_lshlrev_b32_e32 v54, 16, v56
	v_and_b32_e32 v55, 0xffff0000, v56
	v_lshlrev_b32_e32 v66, 16, v58
	v_and_b32_e32 v67, 0xffff0000, v58
	v_pk_fma_f32 v[50:51], v[50:51], v[54:55], v[66:67]
	v_lshlrev_b64 v[54:55], 12, v[60:61]
	v_lshlrev_b32_e32 v56, 16, v57
	v_and_b32_e32 v57, 0xffff0000, v57
	v_lshlrev_b32_e32 v58, 16, v59
	v_and_b32_e32 v59, 0xffff0000, v59
	v_lshl_add_u64 v[54:55], s[10:11], 0, v[54:55]
	v_addc_co_u32_e32 v65, vcc, 0, v63, vcc
	v_pk_fma_f32 v[52:53], v[52:53], v[56:57], v[58:59]
	v_lshl_add_u64 v[54:55], v[54:55], 0, v[142:143]
	v_cvt_pk_bf16_f32 v50, v50, v51
	v_cvt_pk_bf16_f32 v51, v52, v53
	v_mov_b32_e32 v52, v208
	v_mov_b32_e32 v53, v209
	v_mov_b32_e32 v56, v210
	v_mov_b32_e32 v57, v211
	v_lshl_add_u64 v[58:59], v[62:63], 0, s[12:13]
	global_store_dwordx2 v[70:71], v[50:51], off offset:288
	s_nop 0
	v_lshlrev_b32_e32 v50, 16, v52
	v_and_b32_e32 v51, 0xffff0000, v52
	v_lshlrev_b32_e32 v52, 16, v53
	v_and_b32_e32 v53, 0xffff0000, v53
	v_lshlrev_b32_e32 v60, 16, v56
	v_and_b32_e32 v61, 0xffff0000, v56
	v_lshlrev_b32_e32 v56, 16, v57
	v_and_b32_e32 v57, 0xffff0000, v57
	v_pk_fma_f32 v[48:49], v[48:49], v[52:53], v[56:57]
	v_pk_fma_f32 v[46:47], v[46:47], v[50:51], v[60:61]
	s_nop 0
	v_cvt_pk_bf16_f32 v46, v46, v47
	v_cvt_pk_bf16_f32 v47, v48, v49
	v_mov_b32_e32 v48, v212
	v_mov_b32_e32 v49, v213
	v_mov_b32_e32 v50, v214
	v_mov_b32_e32 v51, v215
	s_nop 0
	v_lshlrev_b32_e32 v52, 16, v50
	global_store_dwordx2 v[54:55], v[46:47], off
	v_lshlrev_b32_e32 v46, 16, v48
	v_and_b32_e32 v47, 0xffff0000, v48
	v_lshlrev_b32_e32 v48, 16, v49
	v_and_b32_e32 v49, 0xffff0000, v49
	v_and_b32_e32 v53, 0xffff0000, v50
	v_lshlrev_b32_e32 v50, 16, v51
	v_and_b32_e32 v51, 0xffff0000, v51
	v_pk_fma_f32 v[44:45], v[44:45], v[48:49], v[50:51]
	v_pk_fma_f32 v[42:43], v[42:43], v[46:47], v[52:53]
	s_nop 0
	v_cvt_pk_bf16_f32 v42, v42, v43
	v_cvt_pk_bf16_f32 v43, v44, v45
	v_mov_b32_e32 v44, v216
	v_mov_b32_e32 v45, v217
	v_mov_b32_e32 v46, v218
	v_mov_b32_e32 v47, v219
	s_nop 0
	v_lshlrev_b32_e32 v48, 16, v46
	global_store_dwordx2 v[54:55], v[42:43], off offset:32
	v_lshlrev_b32_e32 v42, 16, v44
	v_and_b32_e32 v43, 0xffff0000, v44
	v_lshlrev_b32_e32 v44, 16, v45
	v_and_b32_e32 v45, 0xffff0000, v45
	v_and_b32_e32 v49, 0xffff0000, v46
	v_lshlrev_b32_e32 v46, 16, v47
	v_and_b32_e32 v47, 0xffff0000, v47
	v_pk_fma_f32 v[40:41], v[40:41], v[44:45], v[46:47]
	v_pk_fma_f32 v[38:39], v[38:39], v[42:43], v[48:49]
	v_add_u32_e32 v44, 0xa0, v144
	v_cvt_pk_bf16_f32 v38, v38, v39
	v_cvt_pk_bf16_f32 v39, v40, v41
	v_mov_b32_e32 v40, v220
	v_mov_b32_e32 v41, v221
	v_mov_b32_e32 v42, v222
	v_mov_b32_e32 v43, v223
	v_ashrrev_i32_e32 v45, 31, v44
	v_mad_i64_i32 v[46:47], s[24:25], v44, s50, v[146:147]
	global_store_dwordx2 v[54:55], v[38:39], off offset:256
	v_lshl_add_u64 v[46:47], v[46:47], 0, v[142:143]
	v_add_co_u32_e32 v48, vcc, s51, v46
	s_nop 0
	v_lshlrev_b32_e32 v38, 16, v40
	v_and_b32_e32 v39, 0xffff0000, v40
	v_lshlrev_b32_e32 v50, 16, v42
	v_and_b32_e32 v51, 0xffff0000, v42
	v_pk_fma_f32 v[34:35], v[34:35], v[38:39], v[50:51]
	v_lshlrev_b64 v[38:39], 12, v[44:45]
	v_lshlrev_b32_e32 v40, 16, v41
	v_and_b32_e32 v41, 0xffff0000, v41
	v_lshlrev_b32_e32 v42, 16, v43
	v_and_b32_e32 v43, 0xffff0000, v43
	v_lshl_add_u64 v[38:39], s[10:11], 0, v[38:39]
	v_addc_co_u32_e32 v49, vcc, 0, v47, vcc
	v_pk_fma_f32 v[36:37], v[36:37], v[40:41], v[42:43]
	v_lshl_add_u64 v[38:39], v[38:39], 0, v[142:143]
	v_cvt_pk_bf16_f32 v34, v34, v35
	v_cvt_pk_bf16_f32 v35, v36, v37
	v_mov_b32_e32 v237, 0x1000
	v_mov_b32_e32 v236, 160
	v_mad_i64_i32 v[230:231], s[24:25], v236, s50, v[228:229]
	v_mad_i64_i32 v[234:235], s[24:25], v236, v237, v[232:233]
	global_load_dwordx2 v[174:175], v[230:231], off
	global_load_dwordx2 v[176:177], v[234:235], off
	global_load_dwordx2 v[178:179], v[230:231], off offset:32
	global_load_dwordx2 v[180:181], v[234:235], off offset:32
	global_load_dwordx2 v[182:183], v[230:231], off offset:256
	global_load_dwordx2 v[184:185], v[234:235], off offset:256
	global_load_dwordx2 v[186:187], v[230:231], off offset:288
	global_load_dwordx2 v[188:189], v[234:235], off offset:288
	v_mov_b32_e32 v236, 176
	v_mad_i64_i32 v[230:231], s[24:25], v236, s50, v[228:229]
	v_mad_i64_i32 v[234:235], s[24:25], v236, v237, v[232:233]
	global_load_dwordx2 v[192:193], v[230:231], off
	global_load_dwordx2 v[194:195], v[234:235], off
	global_load_dwordx2 v[196:197], v[230:231], off offset:32
	global_load_dwordx2 v[198:199], v[234:235], off offset:32
	global_load_dwordx2 v[200:201], v[230:231], off offset:256
	global_load_dwordx2 v[202:203], v[234:235], off offset:256
	global_load_dwordx2 v[204:205], v[230:231], off offset:288
	global_load_dwordx2 v[206:207], v[234:235], off offset:288
	s_waitcnt vmcnt(0)
	v_mov_b32_e32 v36, v174
	v_mov_b32_e32 v37, v175
	v_mov_b32_e32 v40, v176
	v_mov_b32_e32 v41, v177
	v_lshl_add_u64 v[42:43], v[46:47], 0, s[12:13]
	global_store_dwordx2 v[54:55], v[34:35], off offset:288
	s_nop 0
	v_lshlrev_b32_e32 v34, 16, v36
	v_and_b32_e32 v35, 0xffff0000, v36
	v_lshlrev_b32_e32 v36, 16, v37
	v_and_b32_e32 v37, 0xffff0000, v37
	v_lshlrev_b32_e32 v44, 16, v40
	v_and_b32_e32 v45, 0xffff0000, v40
	v_lshlrev_b32_e32 v40, 16, v41
	v_and_b32_e32 v41, 0xffff0000, v41
	v_pk_fma_f32 v[32:33], v[32:33], v[36:37], v[40:41]
	v_pk_fma_f32 v[30:31], v[30:31], v[34:35], v[44:45]
	s_nop 0
	v_cvt_pk_bf16_f32 v30, v30, v31
	v_cvt_pk_bf16_f32 v31, v32, v33
	v_mov_b32_e32 v32, v178
	v_mov_b32_e32 v33, v179
	v_mov_b32_e32 v34, v180
	v_mov_b32_e32 v35, v181
	s_nop 0
	v_lshlrev_b32_e32 v36, 16, v34
	global_store_dwordx2 v[38:39], v[30:31], off
	v_lshlrev_b32_e32 v30, 16, v32
	v_and_b32_e32 v31, 0xffff0000, v32
	v_lshlrev_b32_e32 v32, 16, v33
	v_and_b32_e32 v33, 0xffff0000, v33
	v_and_b32_e32 v37, 0xffff0000, v34
	v_lshlrev_b32_e32 v34, 16, v35
	v_and_b32_e32 v35, 0xffff0000, v35
	v_pk_fma_f32 v[28:29], v[28:29], v[32:33], v[34:35]
	v_pk_fma_f32 v[26:27], v[26:27], v[30:31], v[36:37]
	s_nop 0
	v_cvt_pk_bf16_f32 v26, v26, v27
	v_cvt_pk_bf16_f32 v27, v28, v29
	v_mov_b32_e32 v28, v182
	v_mov_b32_e32 v29, v183
	v_mov_b32_e32 v30, v184
	v_mov_b32_e32 v31, v185
	s_nop 0
	v_lshlrev_b32_e32 v32, 16, v30
	global_store_dwordx2 v[38:39], v[26:27], off offset:32
	v_lshlrev_b32_e32 v26, 16, v28
	v_and_b32_e32 v27, 0xffff0000, v28
	v_lshlrev_b32_e32 v28, 16, v29
	v_and_b32_e32 v29, 0xffff0000, v29
	v_and_b32_e32 v33, 0xffff0000, v30
	v_lshlrev_b32_e32 v30, 16, v31
	v_and_b32_e32 v31, 0xffff0000, v31
	v_pk_fma_f32 v[24:25], v[24:25], v[28:29], v[30:31]
	v_pk_fma_f32 v[22:23], v[22:23], v[26:27], v[32:33]
	v_add_u32_e32 v28, 0xb0, v144
	v_cvt_pk_bf16_f32 v22, v22, v23
	v_cvt_pk_bf16_f32 v23, v24, v25
	v_mov_b32_e32 v24, v186
	v_mov_b32_e32 v25, v187
	v_mov_b32_e32 v26, v188
	v_mov_b32_e32 v27, v189
	v_ashrrev_i32_e32 v29, 31, v28
	v_mad_i64_i32 v[30:31], s[24:25], v28, s50, v[146:147]
	global_store_dwordx2 v[38:39], v[22:23], off offset:256
	v_lshl_add_u64 v[30:31], v[30:31], 0, v[142:143]
	v_add_co_u32_e32 v32, vcc, s51, v30
	s_mov_b64 s[24:25], s[18:19]
	s_nop 0
	v_addc_co_u32_e32 v33, vcc, 0, v31, vcc
	s_and_b64 vcc, exec, s[2:3]
	s_nop 0
	v_lshlrev_b32_e32 v22, 16, v24
	v_and_b32_e32 v23, 0xffff0000, v24
	v_lshlrev_b32_e32 v34, 16, v26
	v_and_b32_e32 v35, 0xffff0000, v26
	v_pk_fma_f32 v[18:19], v[18:19], v[22:23], v[34:35]
	v_lshlrev_b64 v[22:23], 12, v[28:29]
	v_lshlrev_b32_e32 v24, 16, v25
	v_and_b32_e32 v25, 0xffff0000, v25
	v_lshlrev_b32_e32 v26, 16, v27
	v_and_b32_e32 v27, 0xffff0000, v27
	v_lshl_add_u64 v[22:23], s[10:11], 0, v[22:23]
	v_pk_fma_f32 v[20:21], v[20:21], v[24:25], v[26:27]
	v_lshl_add_u64 v[22:23], v[22:23], 0, v[142:143]
	v_cvt_pk_bf16_f32 v18, v18, v19
	v_cvt_pk_bf16_f32 v19, v20, v21
	v_mov_b32_e32 v20, v192
	v_mov_b32_e32 v21, v193
	v_mov_b32_e32 v24, v194
	v_mov_b32_e32 v25, v195
	v_lshl_add_u64 v[26:27], v[30:31], 0, s[12:13]
	global_store_dwordx2 v[38:39], v[18:19], off offset:288
	s_nop 0
	v_lshlrev_b32_e32 v18, 16, v20
	v_and_b32_e32 v19, 0xffff0000, v20
	v_lshlrev_b32_e32 v20, 16, v21
	v_and_b32_e32 v21, 0xffff0000, v21
	v_lshlrev_b32_e32 v28, 16, v24
	v_and_b32_e32 v29, 0xffff0000, v24
	v_lshlrev_b32_e32 v24, 16, v25
	v_and_b32_e32 v25, 0xffff0000, v25
	v_pk_fma_f32 v[16:17], v[16:17], v[20:21], v[24:25]
	v_pk_fma_f32 v[14:15], v[14:15], v[18:19], v[28:29]
	s_nop 0
	v_cvt_pk_bf16_f32 v14, v14, v15
	v_cvt_pk_bf16_f32 v15, v16, v17
	v_mov_b32_e32 v16, v196
	v_mov_b32_e32 v17, v197
	v_mov_b32_e32 v18, v198
	v_mov_b32_e32 v19, v199
	s_nop 0
	v_lshlrev_b32_e32 v20, 16, v18
	global_store_dwordx2 v[22:23], v[14:15], off
	v_lshlrev_b32_e32 v14, 16, v16
	v_and_b32_e32 v15, 0xffff0000, v16
	v_lshlrev_b32_e32 v16, 16, v17
	v_and_b32_e32 v17, 0xffff0000, v17
	v_and_b32_e32 v21, 0xffff0000, v18
	v_lshlrev_b32_e32 v18, 16, v19
	v_and_b32_e32 v19, 0xffff0000, v19
	v_pk_fma_f32 v[12:13], v[12:13], v[16:17], v[18:19]
	v_pk_fma_f32 v[10:11], v[10:11], v[14:15], v[20:21]
	s_nop 0
	v_cvt_pk_bf16_f32 v10, v10, v11
	v_cvt_pk_bf16_f32 v11, v12, v13
	v_mov_b32_e32 v12, v200
	v_mov_b32_e32 v13, v201
	v_mov_b32_e32 v14, v202
	v_mov_b32_e32 v15, v203
	s_nop 0
	v_lshlrev_b32_e32 v16, 16, v14
	global_store_dwordx2 v[22:23], v[10:11], off offset:32
	v_lshlrev_b32_e32 v10, 16, v12
	v_and_b32_e32 v11, 0xffff0000, v12
	v_lshlrev_b32_e32 v12, 16, v13
	v_and_b32_e32 v13, 0xffff0000, v13
	v_and_b32_e32 v17, 0xffff0000, v14
	v_lshlrev_b32_e32 v14, 16, v15
	v_and_b32_e32 v15, 0xffff0000, v15
	v_pk_fma_f32 v[8:9], v[8:9], v[12:13], v[14:15]
	v_pk_fma_f32 v[6:7], v[6:7], v[10:11], v[16:17]
	s_nop 0
	v_cvt_pk_bf16_f32 v6, v6, v7
	v_cvt_pk_bf16_f32 v7, v8, v9
	v_mov_b32_e32 v8, v204
	v_mov_b32_e32 v9, v205
	v_mov_b32_e32 v10, v206
	v_mov_b32_e32 v11, v207
	s_nop 0
	v_lshlrev_b32_e32 v12, 16, v10
	global_store_dwordx2 v[22:23], v[6:7], off offset:256
	v_lshlrev_b32_e32 v6, 16, v8
	v_and_b32_e32 v7, 0xffff0000, v8
	v_and_b32_e32 v13, 0xffff0000, v10
	v_lshlrev_b32_e32 v8, 16, v9
	v_and_b32_e32 v9, 0xffff0000, v9
	v_lshlrev_b32_e32 v10, 16, v11
	v_and_b32_e32 v11, 0xffff0000, v11
	v_pk_fma_f32 v[2:3], v[2:3], v[6:7], v[12:13]
	v_pk_fma_f32 v[4:5], v[4:5], v[8:9], v[10:11]
	v_cvt_pk_bf16_f32 v2, v2, v3
	s_nop 0
	v_cvt_pk_bf16_f32 v3, v4, v5
	global_store_dwordx2 v[22:23], v[2:3], off offset:288
	s_cbranch_vccz .LBB0_1208
	s_waitcnt vmcnt(0)
	s_cmp_lg_u32 s30, 0x100
	s_cbranch_scc1 .Ldt_p1
	s_cmp_lg_u32 s44, 3
	s_cbranch_scc1 .Ldt_p1
	buffer_wbl2 sc1
	s_waitcnt vmcnt(0)
	v_readlane_b32 s92, v250, 40
	v_readlane_b32 s93, v250, 41
	s_sub_i32 s94, s31, 8
	s_lshl_b32 s94, s94, 7
	s_add_i32 s94, s94, 0x10400
	s_add_u32 s92, s92, s94
	s_addc_u32 s93, s93, 0
	v_mov_b32_e32 v2, 0
	v_mov_b32_e32 v3, 1
	s_mov_b64 s[96:97], exec
	s_mov_b64 exec, 1
	global_atomic_add v2, v3, s[92:93]
	s_mov_b64 exec, s[96:97]
	s_waitcnt vmcnt(0)
.Ldt_p1:
	v_readlane_b32 s52, v250, 40
	s_cmpk_gt_u32 s33, 0xff
	v_readlane_b32 s53, v250, 41
	v_readlane_b32 s54, v250, 42
	v_readlane_b32 s55, v250, 43
	s_cbranch_scc1 .LBB0_1215
	s_barrier

.LBB0_1220:
	s_add_i32 s42, s42, 1
	s_mul_i32 s0, s42, s45
	s_mul_hi_u32 s1, s42, s30
	s_add_i32 s1, s1, s0
	s_mul_i32 s0, s42, s30
	s_add_u32 s16, s0, s31
	s_addc_u32 s17, s1, s37
	s_cmp_lg_u32 s30, 0x100
	s_cbranch_scc1 .Ldadj2
	s_cmp_lt_u32 s16, 0x200
	s_cbranch_scc1 .Ldadj2
	s_sub_i32 s16, s16, 16
	s_cmp_lt_u32 s16, 0x200
	s_cselect_b32 s16, 0x7fff, s16
.Ldadj2:
	v_cmp_gt_i64_e64 s[0:1], s[16:17], v[140:141]
	s_and_b64 vcc, exec, s[0:1]
	s_cbranch_vccnz .LBB0_1222
	s_ashr_i32 s12, s16, 31
	s_lshr_b32 s12, s12, 29
	s_add_i32 s12, s16, s12
	s_ashr_i32 s13, s12, 3
	s_and_b32 s12, s12, -8
	s_sub_i32 s12, s16, s12
	s_cmp_lt_i32 s12, 0
	s_cselect_b32 s14, s38, 0x41
	s_mul_i32 s12, s14, s12
	s_add_i32 s12, s12, s13
	s_ashr_i32 s13, s12, 31
	s_lshr_b32 s13, s13, 26
	s_add_i32 s13, s12, s13
	s_ashr_i32 s14, s13, 6
	s_lshl_b32 s14, s14, 3
	s_sub_i32 s15, 0x41, s14
	s_min_i32 s15, s15, 8
	s_abs_i32 s18, s15
	v_cvt_f32_u32_e32 v2, s18
	s_sub_i32 s26, 0, s18
	s_andn2_b32 s13, s13, 63
	s_sub_i32 s13, s12, s13
	v_rcp_iflag_f32_e32 v2, v2
	s_abs_i32 s12, s13
	s_xor_b32 s19, s13, s15
	s_ashr_i32 s19, s19, 31
	v_mul_f32_e32 v2, 0x4f7ffffe, v2
	v_cvt_u32_f32_e32 v2, v2
	s_nop 0
	v_readfirstlane_b32 s27, v2
	s_mul_i32 s26, s26, s27
	s_mul_hi_u32 s26, s27, s26
	s_add_i32 s27, s27, s26
	s_mul_hi_u32 s26, s12, s27
	s_mul_i32 s27, s26, s18
	s_sub_i32 s12, s12, s27
	s_add_i32 s51, s26, 1
	s_sub_i32 s27, s12, s18
	s_cmp_ge_u32 s12, s18
	s_cselect_b32 s26, s51, s26
	s_cselect_b32 s12, s27, s12
	s_add_i32 s27, s26, 1
	s_cmp_ge_u32 s12, s18
	s_cselect_b32 s12, s27, s26
	s_xor_b32 s12, s12, s19
	s_sub_i32 s12, s12, s19
	s_mul_i32 s15, s12, s15
	s_sub_i32 s13, s13, s15
	s_add_i32 s14, s13, s14

.LBB0_1223:
	ds_read_b128 v[142:145], v1
	ds_read_b128 v[156:159], v1 offset:1024
	ds_read_b128 v[160:163], v1 offset:2048
	ds_read_b128 v[164:167], v1 offset:3072
	s_add_u32 s24, s22, 0xfffc0080
	s_addc_u32 s25, s23, -1
	s_cmp_eq_u32 s55, 12
	s_cselect_b32 s27, s15, s25
	s_cselect_b32 s26, s51, s24
	s_cselect_b32 s25, s13, s54
	s_cselect_b32 s24, s52, s53
	v_lshl_add_u64 v[146:147], s[22:23], 0, v[134:135]
	s_add_i32 m0, s21, 0xc000
	ds_read_b128 v[168:171], v148
	ds_read_b128 v[172:175], v148 offset:1024
	ds_read_b128 v[176:179], v148 offset:2048
	ds_read_b128 v[180:183], v148 offset:3072
	ds_read_b128 v[184:187], v148 offset:4096
	ds_read_b128 v[192:195], v148 offset:5120
	ds_read_b128 v[196:199], v148 offset:6144
	ds_read_b128 v[200:203], v148 offset:7168
	global_load_lds_dwordx4 v[146:147], off
	v_lshl_add_u64 v[146:147], s[22:23], 0, v[136:137]
	s_add_i32 m0, s21, 0xe000
	s_nop 0
	global_load_lds_dwordx4 v[146:147], off
	s_waitcnt lgkmcnt(8)
	s_barrier
	s_waitcnt lgkmcnt(0)
	s_setprio 1
	s_waitcnt lgkmcnt(0)
	v_mfma_f32_16x16x32_bf16 v[126:129], v[142:145], v[168:171], v[126:129]
	v_mfma_f32_16x16x32_bf16 v[122:125], v[160:163], v[168:171], v[122:125]
	v_mfma_f32_16x16x32_bf16 v[110:113], v[142:145], v[176:179], v[110:113]
	v_mfma_f32_16x16x32_bf16 v[106:109], v[160:163], v[176:179], v[106:109]
	v_mfma_f32_16x16x32_bf16 v[94:97], v[142:145], v[184:187], v[94:97]
	v_mfma_f32_16x16x32_bf16 v[90:93], v[160:163], v[184:187], v[90:93]
	v_mfma_f32_16x16x32_bf16 v[78:81], v[142:145], v[196:199], v[78:81]
	v_mfma_f32_16x16x32_bf16 v[74:77], v[160:163], v[196:199], v[74:77]
	v_mfma_f32_16x16x32_bf16 v[126:129], v[156:159], v[172:175], v[126:129]
	v_mfma_f32_16x16x32_bf16 v[122:125], v[164:167], v[172:175], v[122:125]
	v_mfma_f32_16x16x32_bf16 v[110:113], v[156:159], v[180:183], v[110:113]
	v_mfma_f32_16x16x32_bf16 v[106:109], v[164:167], v[180:183], v[106:109]
	v_mfma_f32_16x16x32_bf16 v[94:97], v[156:159], v[192:195], v[94:97]
	v_mfma_f32_16x16x32_bf16 v[90:93], v[164:167], v[192:195], v[90:93]
	v_mfma_f32_16x16x32_bf16 v[78:81], v[156:159], v[200:203], v[78:81]
	v_mfma_f32_16x16x32_bf16 v[74:77], v[164:167], v[200:203], v[74:77]
	s_setprio 0
	s_barrier
	s_add_i32 s56, s46, s36
	v_lshl_add_u64 v[146:147], s[24:25], 0, v[130:131]
	s_mov_b32 m0, s56
	ds_read_b128 v[204:207], v149
	ds_read_b128 v[208:211], v149 offset:1024
	ds_read_b128 v[212:215], v149 offset:2048
	ds_read_b128 v[216:219], v149 offset:3072
	global_load_lds_dwordx4 v[146:147], off
	v_lshl_add_u64 v[188:189], s[24:25], 0, v[132:133]
	s_add_i32 m0, s56, 0x2000
	s_nop 0
	global_load_lds_dwordx4 v[188:189], off
	s_barrier
	s_waitcnt lgkmcnt(0)
	s_setprio 1
	s_waitcnt lgkmcnt(0)
	v_mfma_f32_16x16x32_bf16 v[118:121], v[204:207], v[168:171], v[118:121]
	v_mfma_f32_16x16x32_bf16 v[114:117], v[212:215], v[168:171], v[114:117]
	v_mfma_f32_16x16x32_bf16 v[102:105], v[204:207], v[176:179], v[102:105]
	v_mfma_f32_16x16x32_bf16 v[98:101], v[212:215], v[176:179], v[98:101]
	v_mfma_f32_16x16x32_bf16 v[86:89], v[204:207], v[184:187], v[86:89]
	v_mfma_f32_16x16x32_bf16 v[82:85], v[212:215], v[184:187], v[82:85]
	v_mfma_f32_16x16x32_bf16 v[70:73], v[204:207], v[196:199], v[70:73]
	v_mfma_f32_16x16x32_bf16 v[66:69], v[212:215], v[196:199], v[66:69]
	v_mfma_f32_16x16x32_bf16 v[118:121], v[208:211], v[172:175], v[118:121]
	v_mfma_f32_16x16x32_bf16 v[114:117], v[216:219], v[172:175], v[114:117]
	v_mfma_f32_16x16x32_bf16 v[102:105], v[208:211], v[180:183], v[102:105]
	v_mfma_f32_16x16x32_bf16 v[98:101], v[216:219], v[180:183], v[98:101]
	v_mfma_f32_16x16x32_bf16 v[86:89], v[208:211], v[192:195], v[86:89]
	v_mfma_f32_16x16x32_bf16 v[82:85], v[216:219], v[192:195], v[82:85]
	v_mfma_f32_16x16x32_bf16 v[70:73], v[208:211], v[200:203], v[70:73]
	v_mfma_f32_16x16x32_bf16 v[66:69], v[216:219], v[200:203], v[66:69]
	s_setprio 0
	s_mov_b32 m0, s21
	v_lshl_add_u64 v[190:191], s[26:27], 0, v[130:131]
	s_barrier
	ds_read_b128 v[168:171], v148 offset:16384
	ds_read_b128 v[172:175], v148 offset:17408
	ds_read_b128 v[176:179], v148 offset:18432
	ds_read_b128 v[180:183], v148 offset:19456
	ds_read_b128 v[184:187], v148 offset:20480
	ds_read_b128 v[192:195], v148 offset:21504
	ds_read_b128 v[196:199], v148 offset:22528
	ds_read_b128 v[200:203], v148 offset:23552
	global_load_lds_dwordx4 v[190:191], off
	v_lshl_add_u64 v[220:221], s[26:27], 0, v[132:133]
	s_mov_b32 m0, s39
	s_nop 0
	global_load_lds_dwordx4 v[220:221], off
	s_barrier
	s_waitcnt lgkmcnt(0)
	s_setprio 1
	s_waitcnt lgkmcnt(0)
	v_mfma_f32_16x16x32_bf16 v[62:65], v[142:145], v[168:171], v[62:65]
	v_mfma_f32_16x16x32_bf16 v[58:61], v[160:163], v[168:171], v[58:61]
	v_mfma_f32_16x16x32_bf16 v[46:49], v[142:145], v[176:179], v[46:49]
	v_mfma_f32_16x16x32_bf16 v[42:45], v[160:163], v[176:179], v[42:45]
	v_mfma_f32_16x16x32_bf16 v[30:33], v[142:145], v[184:187], v[30:33]
	v_mfma_f32_16x16x32_bf16 v[26:29], v[160:163], v[184:187], v[26:29]
	v_mfma_f32_16x16x32_bf16 v[14:17], v[142:145], v[196:199], v[14:17]
	v_mfma_f32_16x16x32_bf16 v[10:13], v[160:163], v[196:199], v[10:13]
	v_mfma_f32_16x16x32_bf16 v[62:65], v[156:159], v[172:175], v[62:65]
	v_mfma_f32_16x16x32_bf16 v[58:61], v[164:167], v[172:175], v[58:61]
	v_mfma_f32_16x16x32_bf16 v[46:49], v[156:159], v[180:183], v[46:49]
	v_mfma_f32_16x16x32_bf16 v[42:45], v[164:167], v[180:183], v[42:45]
	v_mfma_f32_16x16x32_bf16 v[30:33], v[156:159], v[192:195], v[30:33]
	v_mfma_f32_16x16x32_bf16 v[26:29], v[164:167], v[192:195], v[26:29]
	v_mfma_f32_16x16x32_bf16 v[14:17], v[156:159], v[200:203], v[14:17]
	v_mfma_f32_16x16x32_bf16 v[10:13], v[164:167], v[200:203], v[10:13]
	s_setprio 0
	s_barrier
	s_add_u32 s56, s24, 0x40000
	s_addc_u32 s57, s25, 0
	s_add_i32 s58, s47, s36
	v_lshl_add_u64 v[142:143], s[56:57], 0, v[130:131]
	s_mov_b32 m0, s58
	s_nop 0
	global_load_lds_dwordx4 v[142:143], off
	v_lshl_add_u64 v[142:143], s[56:57], 0, v[132:133]
	s_add_i32 m0, s58, 0x2000
	s_nop 0
	global_load_lds_dwordx4 v[142:143], off
	s_waitcnt vmcnt(6)
	s_barrier
	s_setprio 1
	v_mfma_f32_16x16x32_bf16 v[54:57], v[204:207], v[168:171], v[54:57]
	v_mfma_f32_16x16x32_bf16 v[50:53], v[212:215], v[168:171], v[50:53]
	v_mfma_f32_16x16x32_bf16 v[38:41], v[204:207], v[176:179], v[38:41]
	v_mfma_f32_16x16x32_bf16 v[34:37], v[212:215], v[176:179], v[34:37]
	v_mfma_f32_16x16x32_bf16 v[22:25], v[204:207], v[184:187], v[22:25]
	v_mfma_f32_16x16x32_bf16 v[18:21], v[212:215], v[184:187], v[18:21]
	v_mfma_f32_16x16x32_bf16 v[6:9], v[204:207], v[196:199], v[6:9]
	v_mfma_f32_16x16x32_bf16 v[2:5], v[212:215], v[196:199], v[2:5]
	v_mfma_f32_16x16x32_bf16 v[54:57], v[208:211], v[172:175], v[54:57]
	v_mfma_f32_16x16x32_bf16 v[50:53], v[216:219], v[172:175], v[50:53]
	v_mfma_f32_16x16x32_bf16 v[38:41], v[208:211], v[180:183], v[38:41]
	v_mfma_f32_16x16x32_bf16 v[34:37], v[216:219], v[180:183], v[34:37]
	v_mfma_f32_16x16x32_bf16 v[22:25], v[208:211], v[192:195], v[22:25]
	v_mfma_f32_16x16x32_bf16 v[18:21], v[216:219], v[192:195], v[18:21]
	v_mfma_f32_16x16x32_bf16 v[6:9], v[208:211], v[200:203], v[6:9]
	v_mfma_f32_16x16x32_bf16 v[2:5], v[216:219], v[200:203], v[2:5]
	s_setprio 0
	s_add_i32 s56, 0, 0x18000
	v_add_u32_e32 v150, s56, v152
	s_barrier
	ds_read_b128 v[142:145], v150
	ds_read_b128 v[156:159], v150 offset:1024
	ds_read_b128 v[160:163], v150 offset:2048
	ds_read_b128 v[164:167], v150 offset:3072
	s_add_u32 s26, s26, 0x40000
	s_addc_u32 s27, s27, 0
	s_mov_b32 m0, s40
	v_lshl_add_u64 v[204:205], s[26:27], 0, v[130:131]
	ds_read_b128 v[168:171], v148 offset:32768
	ds_read_b128 v[172:175], v148 offset:33792
	ds_read_b128 v[176:179], v148 offset:34816
	ds_read_b128 v[180:183], v148 offset:35840
	ds_read_b128 v[184:187], v148 offset:36864
	ds_read_b128 v[192:195], v148 offset:37888
	ds_read_b128 v[196:199], v148 offset:38912
	ds_read_b128 v[200:203], v148 offset:39936
	global_load_lds_dwordx4 v[204:205], off
	v_lshl_add_u64 v[204:205], s[26:27], 0, v[132:133]
	s_mov_b32 m0, s41
	s_nop 0
	global_load_lds_dwordx4 v[204:205], off
	s_waitcnt lgkmcnt(8)
	s_barrier
	s_waitcnt lgkmcnt(0)
	s_setprio 1
	s_waitcnt lgkmcnt(0)
	v_mfma_f32_16x16x32_bf16 v[126:129], v[142:145], v[168:171], v[126:129]
	v_mfma_f32_16x16x32_bf16 v[122:125], v[160:163], v[168:171], v[122:125]
	v_mfma_f32_16x16x32_bf16 v[110:113], v[142:145], v[176:179], v[110:113]
	v_mfma_f32_16x16x32_bf16 v[106:109], v[160:163], v[176:179], v[106:109]
	v_mfma_f32_16x16x32_bf16 v[94:97], v[142:145], v[184:187], v[94:97]
	v_mfma_f32_16x16x32_bf16 v[90:93], v[160:163], v[184:187], v[90:93]
	v_mfma_f32_16x16x32_bf16 v[78:81], v[142:145], v[196:199], v[78:81]
	v_mfma_f32_16x16x32_bf16 v[74:77], v[160:163], v[196:199], v[74:77]
	v_mfma_f32_16x16x32_bf16 v[126:129], v[156:159], v[172:175], v[126:129]
	v_mfma_f32_16x16x32_bf16 v[122:125], v[164:167], v[172:175], v[122:125]
	v_mfma_f32_16x16x32_bf16 v[110:113], v[156:159], v[180:183], v[110:113]
	v_mfma_f32_16x16x32_bf16 v[106:109], v[164:167], v[180:183], v[106:109]
	v_mfma_f32_16x16x32_bf16 v[94:97], v[156:159], v[192:195], v[94:97]
	v_mfma_f32_16x16x32_bf16 v[90:93], v[164:167], v[192:195], v[90:93]
	v_mfma_f32_16x16x32_bf16 v[78:81], v[156:159], v[200:203], v[78:81]
	v_mfma_f32_16x16x32_bf16 v[74:77], v[164:167], v[200:203], v[74:77]
	s_setprio 0
	s_barrier
	s_add_i32 s26, 0, 0x1c000
	s_add_i32 s27, s56, s36
	v_add_u32_e32 v150, s26, v152
	v_lshl_add_u64 v[146:147], v[146:147], 0, s[2:3]
	s_mov_b32 m0, s27
	ds_read_b128 v[204:207], v150
	ds_read_b128 v[208:211], v150 offset:1024
	ds_read_b128 v[212:215], v150 offset:2048
	ds_read_b128 v[216:219], v150 offset:3072
	global_load_lds_dwordx4 v[146:147], off
	v_lshl_add_u64 v[146:147], v[188:189], 0, s[2:3]
	s_add_i32 m0, s27, 0x2000
	s_nop 0
	global_load_lds_dwordx4 v[146:147], off
	s_barrier
	s_waitcnt lgkmcnt(0)
	s_setprio 1
	s_waitcnt lgkmcnt(0)
	v_mfma_f32_16x16x32_bf16 v[118:121], v[204:207], v[168:171], v[118:121]
	v_mfma_f32_16x16x32_bf16 v[114:117], v[212:215], v[168:171], v[114:117]
	v_mfma_f32_16x16x32_bf16 v[102:105], v[204:207], v[176:179], v[102:105]
	v_mfma_f32_16x16x32_bf16 v[98:101], v[212:215], v[176:179], v[98:101]
	v_mfma_f32_16x16x32_bf16 v[86:89], v[204:207], v[184:187], v[86:89]
	v_mfma_f32_16x16x32_bf16 v[82:85], v[212:215], v[184:187], v[82:85]
	v_mfma_f32_16x16x32_bf16 v[70:73], v[204:207], v[196:199], v[70:73]
	v_mfma_f32_16x16x32_bf16 v[66:69], v[212:215], v[196:199], v[66:69]
	v_mfma_f32_16x16x32_bf16 v[118:121], v[208:211], v[172:175], v[118:121]
	v_mfma_f32_16x16x32_bf16 v[114:117], v[216:219], v[172:175], v[114:117]
	v_mfma_f32_16x16x32_bf16 v[102:105], v[208:211], v[180:183], v[102:105]
	v_mfma_f32_16x16x32_bf16 v[98:101], v[216:219], v[180:183], v[98:101]
	v_mfma_f32_16x16x32_bf16 v[86:89], v[208:211], v[192:195], v[86:89]
	v_mfma_f32_16x16x32_bf16 v[82:85], v[216:219], v[192:195], v[82:85]
	v_mfma_f32_16x16x32_bf16 v[70:73], v[208:211], v[200:203], v[70:73]
	v_mfma_f32_16x16x32_bf16 v[66:69], v[216:219], v[200:203], v[66:69]
	s_setprio 0
	s_mov_b32 m0, s43
	v_lshl_add_u64 v[146:147], v[190:191], 0, s[2:3]
	s_barrier
	ds_read_b128 v[168:171], v148 offset:49152
	ds_read_b128 v[172:175], v148 offset:50176
	ds_read_b128 v[176:179], v148 offset:51200
	ds_read_b128 v[180:183], v148 offset:52224
	ds_read_b128 v[184:187], v148 offset:53248
	ds_read_b128 v[192:195], v148 offset:54272
	ds_read_b128 v[196:199], v148 offset:55296
	ds_read_b128 v[200:203], v148 offset:56320
	global_load_lds_dwordx4 v[146:147], off
	v_lshl_add_u64 v[146:147], v[220:221], 0, s[2:3]
	s_mov_b32 m0, s44
	s_nop 0
	global_load_lds_dwordx4 v[146:147], off
	s_barrier
	s_waitcnt lgkmcnt(0)
	s_setprio 1
	s_waitcnt lgkmcnt(0)
	v_mfma_f32_16x16x32_bf16 v[62:65], v[142:145], v[168:171], v[62:65]
	v_mfma_f32_16x16x32_bf16 v[58:61], v[160:163], v[168:171], v[58:61]
	v_mfma_f32_16x16x32_bf16 v[46:49], v[142:145], v[176:179], v[46:49]
	v_mfma_f32_16x16x32_bf16 v[42:45], v[160:163], v[176:179], v[42:45]
	v_mfma_f32_16x16x32_bf16 v[30:33], v[142:145], v[184:187], v[30:33]
	v_mfma_f32_16x16x32_bf16 v[26:29], v[160:163], v[184:187], v[26:29]
	v_mfma_f32_16x16x32_bf16 v[14:17], v[142:145], v[196:199], v[14:17]
	v_mfma_f32_16x16x32_bf16 v[10:13], v[160:163], v[196:199], v[10:13]
	v_mfma_f32_16x16x32_bf16 v[62:65], v[156:159], v[172:175], v[62:65]
	v_mfma_f32_16x16x32_bf16 v[58:61], v[164:167], v[172:175], v[58:61]
	v_mfma_f32_16x16x32_bf16 v[46:49], v[156:159], v[180:183], v[46:49]
	v_mfma_f32_16x16x32_bf16 v[42:45], v[164:167], v[180:183], v[42:45]
	v_mfma_f32_16x16x32_bf16 v[30:33], v[156:159], v[192:195], v[30:33]
	v_mfma_f32_16x16x32_bf16 v[26:29], v[164:167], v[192:195], v[26:29]
	v_mfma_f32_16x16x32_bf16 v[14:17], v[156:159], v[200:203], v[14:17]
	v_mfma_f32_16x16x32_bf16 v[10:13], v[164:167], v[200:203], v[10:13]
	s_setprio 0
	s_barrier
	s_add_u32 s24, s24, 0x40080
	s_addc_u32 s25, s25, 0
	s_add_i32 s26, s26, s36
	v_lshl_add_u64 v[142:143], s[24:25], 0, v[130:131]
	s_mov_b32 m0, s26
	s_nop 0
	global_load_lds_dwordx4 v[142:143], off
	v_lshl_add_u64 v[142:143], s[24:25], 0, v[132:133]
	s_add_i32 m0, s26, 0x2000
	s_nop 0
	global_load_lds_dwordx4 v[142:143], off
	s_waitcnt vmcnt(6)
	s_barrier
	s_setprio 1
	v_mfma_f32_16x16x32_bf16 v[54:57], v[204:207], v[168:171], v[54:57]
	v_mfma_f32_16x16x32_bf16 v[50:53], v[212:215], v[168:171], v[50:53]
	v_mfma_f32_16x16x32_bf16 v[38:41], v[204:207], v[176:179], v[38:41]
	v_mfma_f32_16x16x32_bf16 v[34:37], v[212:215], v[176:179], v[34:37]
	v_mfma_f32_16x16x32_bf16 v[22:25], v[204:207], v[184:187], v[22:25]
	v_mfma_f32_16x16x32_bf16 v[18:21], v[212:215], v[184:187], v[18:21]
	v_mfma_f32_16x16x32_bf16 v[6:9], v[204:207], v[196:199], v[6:9]
	v_mfma_f32_16x16x32_bf16 v[2:5], v[212:215], v[196:199], v[2:5]
	v_mfma_f32_16x16x32_bf16 v[54:57], v[208:211], v[172:175], v[54:57]
	v_mfma_f32_16x16x32_bf16 v[50:53], v[216:219], v[172:175], v[50:53]
	v_mfma_f32_16x16x32_bf16 v[38:41], v[208:211], v[180:183], v[38:41]
	v_mfma_f32_16x16x32_bf16 v[34:37], v[216:219], v[180:183], v[34:37]
	v_mfma_f32_16x16x32_bf16 v[22:25], v[208:211], v[192:195], v[22:25]
	v_mfma_f32_16x16x32_bf16 v[18:21], v[216:219], v[192:195], v[18:21]
	v_mfma_f32_16x16x32_bf16 v[6:9], v[208:211], v[200:203], v[6:9]
	v_mfma_f32_16x16x32_bf16 v[2:5], v[216:219], v[200:203], v[2:5]
	s_setprio 0
	s_add_i32 s55, s55, 2
	s_add_u32 s22, s22, 0x100
	s_addc_u32 s23, s23, 0
	s_add_u32 s53, s53, 0x100
	s_addc_u32 s54, s54, 0
	s_cmp_gt_u32 s55, 13
	s_barrier
	s_cbranch_scc0 .LBB0_1223
	s_cmp_lg_u32 s30, 0x100
	s_cbranch_scc1 .Ldt_c2
	s_cmp_lg_u32 s42, 3
	s_cbranch_scc1 .Ldt_c2
	v_readlane_b32 s92, v250, 40
	v_readlane_b32 s93, v250, 41
	s_sub_i32 s94, s31, 16
	s_lshl_b32 s94, s94, 7
	s_add_i32 s94, s94, 0x10400
	s_add_u32 s92, s92, s94
	s_addc_u32 s93, s93, 0
	s_mov_b32 s95, 0
	v_mov_b32_e32 v142, 0

.Ldt_c2:
	v_lshl_or_b32 v142, s50, 8, v151
	v_lshl_add_u32 v144, s20, 8, v155
	v_ashrrev_i32_e32 v143, 31, v142
	v_mov_b64_e32 v[146:147], s[6:7]
	v_ashrrev_i32_e32 v145, 31, v144
	v_mad_i64_i32 v[156:157], s[22:23], v144, s48, v[146:147]
	v_lshlrev_b64 v[142:143], 1, v[142:143]
	v_lshl_add_u64 v[156:157], v[156:157], 0, v[142:143]
	v_lshlrev_b64 v[160:161], 12, v[144:145]
	v_add_co_u32_e32 v158, vcc, 0x2ec42000, v156
	v_lshl_add_u64 v[160:161], s[8:9], 0, v[160:161]
	s_nop 0
	v_addc_co_u32_e32 v159, vcc, 0, v157, vcc
	v_lshl_add_u64 v[160:161], v[160:161], 0, v[142:143]
	v_mov_b32_e32 v228, v158
	v_mov_b32_e32 v229, v159
	v_mov_b32_e32 v232, v160
	v_mov_b32_e32 v233, v161
	v_mov_b32_e32 v237, 0x1000
	global_load_dwordx2 v[168:169], v[228:229], off
	global_load_dwordx2 v[170:171], v[232:233], off
	global_load_dwordx2 v[172:173], v[228:229], off offset:32
	global_load_dwordx2 v[174:175], v[232:233], off offset:32
	global_load_dwordx2 v[176:177], v[228:229], off offset:256
	global_load_dwordx2 v[178:179], v[232:233], off offset:256
	global_load_dwordx2 v[180:181], v[228:229], off offset:288
	global_load_dwordx2 v[182:183], v[232:233], off offset:288
	v_mov_b32_e32 v236, 16
	v_mad_i64_i32 v[230:231], s[22:23], v236, s48, v[228:229]
	v_mad_i64_i32 v[234:235], s[22:23], v236, v237, v[232:233]
	global_load_dwordx2 v[184:185], v[230:231], off
	global_load_dwordx2 v[186:187], v[234:235], off
	global_load_dwordx2 v[192:193], v[230:231], off offset:32
	global_load_dwordx2 v[194:195], v[234:235], off offset:32
	global_load_dwordx2 v[196:197], v[230:231], off offset:256
	global_load_dwordx2 v[198:199], v[234:235], off offset:256
	global_load_dwordx2 v[200:201], v[230:231], off offset:288
	global_load_dwordx2 v[202:203], v[234:235], off offset:288
	v_mov_b32_e32 v236, 32
	v_mad_i64_i32 v[230:231], s[22:23], v236, s48, v[228:229]
	v_mad_i64_i32 v[234:235], s[22:23], v236, v237, v[232:233]
	global_load_dwordx2 v[204:205], v[230:231], off
	global_load_dwordx2 v[206:207], v[234:235], off
	global_load_dwordx2 v[208:209], v[230:231], off offset:32
	global_load_dwordx2 v[210:211], v[234:235], off offset:32
	global_load_dwordx2 v[212:213], v[230:231], off offset:256
	global_load_dwordx2 v[214:215], v[234:235], off offset:256
	global_load_dwordx2 v[216:217], v[230:231], off offset:288
	global_load_dwordx2 v[218:219], v[234:235], off offset:288
	s_waitcnt vmcnt(0)
	v_mov_b32_e32 v158, v168
	v_mov_b32_e32 v159, v169
	v_lshl_add_u64 v[156:157], v[156:157], 0, s[10:11]
	v_mov_b32_e32 v162, v170
	v_mov_b32_e32 v163, v171
	s_mov_b32 s50, s12
	s_mov_b32 s20, s14
	s_mov_b64 s[24:25], s[18:19]
	s_nop 0
	v_lshlrev_b32_e32 v164, 16, v158
	v_and_b32_e32 v165, 0xffff0000, v158
	v_lshlrev_b32_e32 v158, 16, v159
	v_and_b32_e32 v159, 0xffff0000, v159
	v_lshlrev_b32_e32 v166, 16, v162
	v_and_b32_e32 v167, 0xffff0000, v162
	v_lshlrev_b32_e32 v162, 16, v163
	v_and_b32_e32 v163, 0xffff0000, v163
	v_pk_fma_f32 v[128:129], v[128:129], v[158:159], v[162:163]
	v_pk_fma_f32 v[126:127], v[126:127], v[164:165], v[166:167]
	s_nop 0
	v_cvt_pk_bf16_f32 v126, v126, v127
	v_cvt_pk_bf16_f32 v127, v128, v129
	v_mov_b32_e32 v128, v172
	v_mov_b32_e32 v129, v173
	v_mov_b32_e32 v158, v174
	v_mov_b32_e32 v159, v175
	s_nop 0
	v_lshlrev_b32_e32 v162, 16, v158
	global_store_dwordx2 v[160:161], v[126:127], off
	v_lshlrev_b32_e32 v126, 16, v128
	v_and_b32_e32 v127, 0xffff0000, v128
	v_lshlrev_b32_e32 v128, 16, v129
	v_and_b32_e32 v129, 0xffff0000, v129
	v_and_b32_e32 v163, 0xffff0000, v158
	v_lshlrev_b32_e32 v158, 16, v159
	v_and_b32_e32 v159, 0xffff0000, v159
	v_pk_fma_f32 v[124:125], v[124:125], v[128:129], v[158:159]
	v_pk_fma_f32 v[122:123], v[122:123], v[126:127], v[162:163]
	s_nop 0
	v_cvt_pk_bf16_f32 v122, v122, v123
	v_cvt_pk_bf16_f32 v123, v124, v125
	v_mov_b32_e32 v124, v176
	v_mov_b32_e32 v125, v177
	v_mov_b32_e32 v126, v178
	v_mov_b32_e32 v127, v179
	s_nop 0
	v_lshlrev_b32_e32 v128, 16, v126
	global_store_dwordx2 v[160:161], v[122:123], off offset:32
	v_lshlrev_b32_e32 v122, 16, v124
	v_and_b32_e32 v123, 0xffff0000, v124
	v_lshlrev_b32_e32 v124, 16, v125
	v_and_b32_e32 v125, 0xffff0000, v125
	v_and_b32_e32 v129, 0xffff0000, v126
	v_lshlrev_b32_e32 v126, 16, v127
	v_and_b32_e32 v127, 0xffff0000, v127
	v_pk_fma_f32 v[120:121], v[120:121], v[124:125], v[126:127]
	v_pk_fma_f32 v[118:119], v[118:119], v[122:123], v[128:129]
	v_or_b32_e32 v124, 16, v144
	v_cvt_pk_bf16_f32 v118, v118, v119
	v_cvt_pk_bf16_f32 v119, v120, v121
	v_mov_b32_e32 v120, v180
	v_mov_b32_e32 v121, v181
	v_mov_b32_e32 v122, v182
	v_mov_b32_e32 v123, v183
	v_ashrrev_i32_e32 v125, 31, v124
	v_mad_i64_i32 v[126:127], s[22:23], v124, s48, v[146:147]
	global_store_dwordx2 v[160:161], v[118:119], off offset:256
	v_lshl_add_u64 v[126:127], v[126:127], 0, v[142:143]
	v_add_co_u32_e32 v128, vcc, s49, v126
	s_nop 0
	v_lshlrev_b32_e32 v118, 16, v120
	v_and_b32_e32 v119, 0xffff0000, v120
	v_lshlrev_b32_e32 v156, 16, v122
	v_and_b32_e32 v157, 0xffff0000, v122
	v_pk_fma_f32 v[114:115], v[114:115], v[118:119], v[156:157]
	v_lshlrev_b64 v[118:119], 12, v[124:125]
	v_lshlrev_b32_e32 v120, 16, v121
	v_and_b32_e32 v121, 0xffff0000, v121
	v_lshlrev_b32_e32 v122, 16, v123
	v_and_b32_e32 v123, 0xffff0000, v123
	v_lshl_add_u64 v[118:119], s[8:9], 0, v[118:119]
	v_addc_co_u32_e32 v129, vcc, 0, v127, vcc
	v_pk_fma_f32 v[116:117], v[116:117], v[120:121], v[122:123]
	v_lshl_add_u64 v[118:119], v[118:119], 0, v[142:143]
	v_cvt_pk_bf16_f32 v114, v114, v115
	v_cvt_pk_bf16_f32 v115, v116, v117
	v_mov_b32_e32 v116, v184
	v_mov_b32_e32 v117, v185
	v_mov_b32_e32 v120, v186
	v_mov_b32_e32 v121, v187
	v_lshl_add_u64 v[122:123], v[126:127], 0, s[10:11]
	global_store_dwordx2 v[160:161], v[114:115], off offset:288
	s_nop 0
	v_lshlrev_b32_e32 v114, 16, v116
	v_and_b32_e32 v115, 0xffff0000, v116
	v_lshlrev_b32_e32 v116, 16, v117
	v_and_b32_e32 v117, 0xffff0000, v117
	v_lshlrev_b32_e32 v124, 16, v120
	v_and_b32_e32 v125, 0xffff0000, v120
	v_lshlrev_b32_e32 v120, 16, v121
	v_and_b32_e32 v121, 0xffff0000, v121
	v_pk_fma_f32 v[112:113], v[112:113], v[116:117], v[120:121]
	v_pk_fma_f32 v[110:111], v[110:111], v[114:115], v[124:125]
	s_nop 0
	v_cvt_pk_bf16_f32 v110, v110, v111
	v_cvt_pk_bf16_f32 v111, v112, v113
	v_mov_b32_e32 v112, v192
	v_mov_b32_e32 v113, v193
	v_mov_b32_e32 v114, v194
	v_mov_b32_e32 v115, v195
	s_nop 0
	v_lshlrev_b32_e32 v116, 16, v114
	global_store_dwordx2 v[118:119], v[110:111], off
	v_lshlrev_b32_e32 v110, 16, v112
	v_and_b32_e32 v111, 0xffff0000, v112
	v_lshlrev_b32_e32 v112, 16, v113
	v_and_b32_e32 v113, 0xffff0000, v113
	v_and_b32_e32 v117, 0xffff0000, v114
	v_lshlrev_b32_e32 v114, 16, v115
	v_and_b32_e32 v115, 0xffff0000, v115
	v_pk_fma_f32 v[108:109], v[108:109], v[112:113], v[114:115]
	v_pk_fma_f32 v[106:107], v[106:107], v[110:111], v[116:117]
	s_nop 0
	v_cvt_pk_bf16_f32 v106, v106, v107
	v_cvt_pk_bf16_f32 v107, v108, v109
	v_mov_b32_e32 v108, v196
	v_mov_b32_e32 v109, v197
	v_mov_b32_e32 v110, v198
	v_mov_b32_e32 v111, v199
	s_nop 0
	v_lshlrev_b32_e32 v112, 16, v110
	global_store_dwordx2 v[118:119], v[106:107], off offset:32
	v_lshlrev_b32_e32 v106, 16, v108
	v_and_b32_e32 v107, 0xffff0000, v108
	v_lshlrev_b32_e32 v108, 16, v109
	v_and_b32_e32 v109, 0xffff0000, v109
	v_and_b32_e32 v113, 0xffff0000, v110
	v_lshlrev_b32_e32 v110, 16, v111
	v_and_b32_e32 v111, 0xffff0000, v111
	v_pk_fma_f32 v[104:105], v[104:105], v[108:109], v[110:111]
	v_pk_fma_f32 v[102:103], v[102:103], v[106:107], v[112:113]
	v_or_b32_e32 v108, 32, v144
	v_cvt_pk_bf16_f32 v102, v102, v103
	v_cvt_pk_bf16_f32 v103, v104, v105
	v_mov_b32_e32 v104, v200
	v_mov_b32_e32 v105, v201
	v_mov_b32_e32 v106, v202
	v_mov_b32_e32 v107, v203
	v_ashrrev_i32_e32 v109, 31, v108
	v_mad_i64_i32 v[110:111], s[22:23], v108, s48, v[146:147]
	global_store_dwordx2 v[118:119], v[102:103], off offset:256
	v_lshl_add_u64 v[110:111], v[110:111], 0, v[142:143]
	v_add_co_u32_e32 v112, vcc, s49, v110
	s_nop 0
	v_lshlrev_b32_e32 v102, 16, v104
	v_and_b32_e32 v103, 0xffff0000, v104
	v_lshlrev_b32_e32 v114, 16, v106
	v_and_b32_e32 v115, 0xffff0000, v106
	v_pk_fma_f32 v[98:99], v[98:99], v[102:103], v[114:115]
	v_lshlrev_b64 v[102:103], 12, v[108:109]
	v_lshlrev_b32_e32 v104, 16, v105
	v_and_b32_e32 v105, 0xffff0000, v105
	v_lshlrev_b32_e32 v106, 16, v107
	v_and_b32_e32 v107, 0xffff0000, v107
	v_lshl_add_u64 v[102:103], s[8:9], 0, v[102:103]
	v_addc_co_u32_e32 v113, vcc, 0, v111, vcc
	v_pk_fma_f32 v[100:101], v[100:101], v[104:105], v[106:107]
	v_lshl_add_u64 v[102:103], v[102:103], 0, v[142:143]
	v_cvt_pk_bf16_f32 v98, v98, v99
	v_cvt_pk_bf16_f32 v99, v100, v101
	v_mov_b32_e32 v100, v204
	v_mov_b32_e32 v101, v205
	v_mov_b32_e32 v104, v206
	v_mov_b32_e32 v105, v207
	v_lshl_add_u64 v[106:107], v[110:111], 0, s[10:11]
	global_store_dwordx2 v[118:119], v[98:99], off offset:288
	s_nop 0
	v_lshlrev_b32_e32 v98, 16, v100
	v_and_b32_e32 v99, 0xffff0000, v100
	v_lshlrev_b32_e32 v100, 16, v101
	v_and_b32_e32 v101, 0xffff0000, v101
	v_lshlrev_b32_e32 v108, 16, v104
	v_and_b32_e32 v109, 0xffff0000, v104
	v_lshlrev_b32_e32 v104, 16, v105
	v_and_b32_e32 v105, 0xffff0000, v105
	v_pk_fma_f32 v[96:97], v[96:97], v[100:101], v[104:105]
	v_pk_fma_f32 v[94:95], v[94:95], v[98:99], v[108:109]
	s_nop 0
	v_cvt_pk_bf16_f32 v94, v94, v95
	v_cvt_pk_bf16_f32 v95, v96, v97
	v_mov_b32_e32 v96, v208
	v_mov_b32_e32 v97, v209
	v_mov_b32_e32 v98, v210
	v_mov_b32_e32 v99, v211
	s_nop 0
	v_lshlrev_b32_e32 v100, 16, v98
	global_store_dwordx2 v[102:103], v[94:95], off
	v_lshlrev_b32_e32 v94, 16, v96
	v_and_b32_e32 v95, 0xffff0000, v96
	v_lshlrev_b32_e32 v96, 16, v97
	v_and_b32_e32 v97, 0xffff0000, v97
	v_and_b32_e32 v101, 0xffff0000, v98
	v_lshlrev_b32_e32 v98, 16, v99
	v_and_b32_e32 v99, 0xffff0000, v99
	v_pk_fma_f32 v[92:93], v[92:93], v[96:97], v[98:99]
	v_pk_fma_f32 v[90:91], v[90:91], v[94:95], v[100:101]
	s_nop 0
	v_cvt_pk_bf16_f32 v90, v90, v91
	v_cvt_pk_bf16_f32 v91, v92, v93
	v_mov_b32_e32 v92, v212
	v_mov_b32_e32 v93, v213
	v_mov_b32_e32 v94, v214
	v_mov_b32_e32 v95, v215
	s_nop 0
	v_lshlrev_b32_e32 v96, 16, v94
	global_store_dwordx2 v[102:103], v[90:91], off offset:32
	v_lshlrev_b32_e32 v90, 16, v92
	v_and_b32_e32 v91, 0xffff0000, v92
	v_lshlrev_b32_e32 v92, 16, v93
	v_and_b32_e32 v93, 0xffff0000, v93
	v_and_b32_e32 v97, 0xffff0000, v94
	v_lshlrev_b32_e32 v94, 16, v95
	v_and_b32_e32 v95, 0xffff0000, v95
	v_pk_fma_f32 v[88:89], v[88:89], v[92:93], v[94:95]
	v_pk_fma_f32 v[86:87], v[86:87], v[90:91], v[96:97]
	v_or_b32_e32 v92, 48, v144
	v_cvt_pk_bf16_f32 v86, v86, v87
	v_cvt_pk_bf16_f32 v87, v88, v89
	v_mov_b32_e32 v88, v216
	v_mov_b32_e32 v89, v217
	v_mov_b32_e32 v90, v218
	v_mov_b32_e32 v91, v219
	v_ashrrev_i32_e32 v93, 31, v92
	v_mad_i64_i32 v[94:95], s[22:23], v92, s48, v[146:147]
	global_store_dwordx2 v[102:103], v[86:87], off offset:256
	v_lshl_add_u64 v[94:95], v[94:95], 0, v[142:143]
	v_add_co_u32_e32 v96, vcc, s49, v94
	s_nop 0
	v_lshlrev_b32_e32 v86, 16, v88
	v_and_b32_e32 v87, 0xffff0000, v88
	v_lshlrev_b32_e32 v98, 16, v90
	v_and_b32_e32 v99, 0xffff0000, v90
	v_pk_fma_f32 v[82:83], v[82:83], v[86:87], v[98:99]
	v_lshlrev_b64 v[86:87], 12, v[92:93]
	v_lshlrev_b32_e32 v88, 16, v89
	v_and_b32_e32 v89, 0xffff0000, v89
	v_lshlrev_b32_e32 v90, 16, v91
	v_and_b32_e32 v91, 0xffff0000, v91
	v_lshl_add_u64 v[86:87], s[8:9], 0, v[86:87]
	v_addc_co_u32_e32 v97, vcc, 0, v95, vcc
	v_pk_fma_f32 v[84:85], v[84:85], v[88:89], v[90:91]
	v_lshl_add_u64 v[86:87], v[86:87], 0, v[142:143]
	v_cvt_pk_bf16_f32 v82, v82, v83
	v_cvt_pk_bf16_f32 v83, v84, v85
	v_mov_b32_e32 v237, 0x1000
	v_mov_b32_e32 v236, 48
	v_mad_i64_i32 v[230:231], s[22:23], v236, s48, v[228:229]
	v_mad_i64_i32 v[234:235], s[22:23], v236, v237, v[232:233]
	global_load_dwordx2 v[168:169], v[230:231], off
	global_load_dwordx2 v[170:171], v[234:235], off
	global_load_dwordx2 v[172:173], v[230:231], off offset:32
	global_load_dwordx2 v[174:175], v[234:235], off offset:32
	global_load_dwordx2 v[176:177], v[230:231], off offset:256
	global_load_dwordx2 v[178:179], v[234:235], off offset:256
	global_load_dwordx2 v[180:181], v[230:231], off offset:288
	global_load_dwordx2 v[182:183], v[234:235], off offset:288
	v_mov_b32_e32 v236, 128
	v_mad_i64_i32 v[230:231], s[22:23], v236, s48, v[228:229]
	v_mad_i64_i32 v[234:235], s[22:23], v236, v237, v[232:233]
	global_load_dwordx2 v[184:185], v[230:231], off
	global_load_dwordx2 v[186:187], v[234:235], off
	global_load_dwordx2 v[192:193], v[230:231], off offset:32
	global_load_dwordx2 v[194:195], v[234:235], off offset:32
	global_load_dwordx2 v[196:197], v[230:231], off offset:256
	global_load_dwordx2 v[198:199], v[234:235], off offset:256
	global_load_dwordx2 v[200:201], v[230:231], off offset:288
	global_load_dwordx2 v[202:203], v[234:235], off offset:288
	v_mov_b32_e32 v236, 144
	v_mad_i64_i32 v[230:231], s[22:23], v236, s48, v[228:229]
	v_mad_i64_i32 v[234:235], s[22:23], v236, v237, v[232:233]
	global_load_dwordx2 v[204:205], v[230:231], off
	global_load_dwordx2 v[206:207], v[234:235], off
	global_load_dwordx2 v[208:209], v[230:231], off offset:32
	global_load_dwordx2 v[210:211], v[234:235], off offset:32
	global_load_dwordx2 v[212:213], v[230:231], off offset:256
	global_load_dwordx2 v[214:215], v[234:235], off offset:256
	global_load_dwordx2 v[216:217], v[230:231], off offset:288
	global_load_dwordx2 v[218:219], v[234:235], off offset:288
	s_waitcnt vmcnt(0)
	v_mov_b32_e32 v84, v168
	v_mov_b32_e32 v85, v169
	v_mov_b32_e32 v88, v170
	v_mov_b32_e32 v89, v171
	v_lshl_add_u64 v[90:91], v[94:95], 0, s[10:11]
	global_store_dwordx2 v[102:103], v[82:83], off offset:288
	s_nop 0
	v_lshlrev_b32_e32 v82, 16, v84
	v_and_b32_e32 v83, 0xffff0000, v84
	v_lshlrev_b32_e32 v84, 16, v85
	v_and_b32_e32 v85, 0xffff0000, v85
	v_lshlrev_b32_e32 v92, 16, v88
	v_and_b32_e32 v93, 0xffff0000, v88
	v_lshlrev_b32_e32 v88, 16, v89
	v_and_b32_e32 v89, 0xffff0000, v89
	v_pk_fma_f32 v[80:81], v[80:81], v[84:85], v[88:89]
	v_pk_fma_f32 v[78:79], v[78:79], v[82:83], v[92:93]
	s_nop 0
	v_cvt_pk_bf16_f32 v78, v78, v79
	v_cvt_pk_bf16_f32 v79, v80, v81
	v_mov_b32_e32 v80, v172
	v_mov_b32_e32 v81, v173
	v_mov_b32_e32 v82, v174
	v_mov_b32_e32 v83, v175
	s_nop 0
	v_lshlrev_b32_e32 v84, 16, v82
	global_store_dwordx2 v[86:87], v[78:79], off
	v_lshlrev_b32_e32 v78, 16, v80
	v_and_b32_e32 v79, 0xffff0000, v80
	v_lshlrev_b32_e32 v80, 16, v81
	v_and_b32_e32 v81, 0xffff0000, v81
	v_and_b32_e32 v85, 0xffff0000, v82
	v_lshlrev_b32_e32 v82, 16, v83
	v_and_b32_e32 v83, 0xffff0000, v83
	v_pk_fma_f32 v[76:77], v[76:77], v[80:81], v[82:83]
	v_pk_fma_f32 v[74:75], v[74:75], v[78:79], v[84:85]
	s_nop 0
	v_cvt_pk_bf16_f32 v74, v74, v75
	v_cvt_pk_bf16_f32 v75, v76, v77
	v_mov_b32_e32 v76, v176
	v_mov_b32_e32 v77, v177
	v_mov_b32_e32 v78, v178
	v_mov_b32_e32 v79, v179
	s_nop 0
	v_lshlrev_b32_e32 v80, 16, v78
	global_store_dwordx2 v[86:87], v[74:75], off offset:32
	v_lshlrev_b32_e32 v74, 16, v76
	v_and_b32_e32 v75, 0xffff0000, v76
	v_lshlrev_b32_e32 v76, 16, v77
	v_and_b32_e32 v77, 0xffff0000, v77
	v_and_b32_e32 v81, 0xffff0000, v78
	v_lshlrev_b32_e32 v78, 16, v79
	v_and_b32_e32 v79, 0xffff0000, v79
	v_pk_fma_f32 v[72:73], v[72:73], v[76:77], v[78:79]
	v_pk_fma_f32 v[70:71], v[70:71], v[74:75], v[80:81]
	v_add_u32_e32 v76, 0x80, v144
	v_cvt_pk_bf16_f32 v70, v70, v71
	v_cvt_pk_bf16_f32 v71, v72, v73
	v_mov_b32_e32 v72, v180
	v_mov_b32_e32 v73, v181
	v_mov_b32_e32 v74, v182
	v_mov_b32_e32 v75, v183
	v_ashrrev_i32_e32 v77, 31, v76
	v_mad_i64_i32 v[78:79], s[22:23], v76, s48, v[146:147]
	global_store_dwordx2 v[86:87], v[70:71], off offset:256
	v_lshl_add_u64 v[78:79], v[78:79], 0, v[142:143]
	v_add_co_u32_e32 v80, vcc, s49, v78
	s_nop 0
	v_lshlrev_b32_e32 v70, 16, v72
	v_and_b32_e32 v71, 0xffff0000, v72
	v_lshlrev_b32_e32 v82, 16, v74
	v_and_b32_e32 v83, 0xffff0000, v74
	v_pk_fma_f32 v[66:67], v[66:67], v[70:71], v[82:83]
	v_lshlrev_b64 v[70:71], 12, v[76:77]
	v_lshlrev_b32_e32 v72, 16, v73
	v_and_b32_e32 v73, 0xffff0000, v73
	v_lshlrev_b32_e32 v74, 16, v75
	v_and_b32_e32 v75, 0xffff0000, v75
	v_lshl_add_u64 v[70:71], s[8:9], 0, v[70:71]
	v_addc_co_u32_e32 v81, vcc, 0, v79, vcc
	v_pk_fma_f32 v[68:69], v[68:69], v[72:73], v[74:75]
	v_lshl_add_u64 v[70:71], v[70:71], 0, v[142:143]
	v_cvt_pk_bf16_f32 v66, v66, v67
	v_cvt_pk_bf16_f32 v67, v68, v69
	v_mov_b32_e32 v68, v184
	v_mov_b32_e32 v69, v185
	v_mov_b32_e32 v72, v186
	v_mov_b32_e32 v73, v187
	v_lshl_add_u64 v[74:75], v[78:79], 0, s[10:11]
	global_store_dwordx2 v[86:87], v[66:67], off offset:288
	s_nop 0
	v_lshlrev_b32_e32 v66, 16, v68
	v_and_b32_e32 v67, 0xffff0000, v68
	v_lshlrev_b32_e32 v68, 16, v69
	v_and_b32_e32 v69, 0xffff0000, v69
	v_lshlrev_b32_e32 v76, 16, v72
	v_and_b32_e32 v77, 0xffff0000, v72
	v_lshlrev_b32_e32 v72, 16, v73
	v_and_b32_e32 v73, 0xffff0000, v73
	v_pk_fma_f32 v[64:65], v[64:65], v[68:69], v[72:73]
	v_pk_fma_f32 v[62:63], v[62:63], v[66:67], v[76:77]
	s_nop 0
	v_cvt_pk_bf16_f32 v62, v62, v63
	v_cvt_pk_bf16_f32 v63, v64, v65
	v_mov_b32_e32 v64, v192
	v_mov_b32_e32 v65, v193
	v_mov_b32_e32 v66, v194
	v_mov_b32_e32 v67, v195
	s_nop 0
	v_lshlrev_b32_e32 v68, 16, v66
	global_store_dwordx2 v[70:71], v[62:63], off
	v_lshlrev_b32_e32 v62, 16, v64
	v_and_b32_e32 v63, 0xffff0000, v64
	v_lshlrev_b32_e32 v64, 16, v65
	v_and_b32_e32 v65, 0xffff0000, v65
	v_and_b32_e32 v69, 0xffff0000, v66
	v_lshlrev_b32_e32 v66, 16, v67
	v_and_b32_e32 v67, 0xffff0000, v67
	v_pk_fma_f32 v[60:61], v[60:61], v[64:65], v[66:67]
	v_pk_fma_f32 v[58:59], v[58:59], v[62:63], v[68:69]
	s_nop 0
	v_cvt_pk_bf16_f32 v58, v58, v59
	v_cvt_pk_bf16_f32 v59, v60, v61
	v_mov_b32_e32 v60, v196
	v_mov_b32_e32 v61, v197
	v_mov_b32_e32 v62, v198
	v_mov_b32_e32 v63, v199
	s_nop 0
	v_lshlrev_b32_e32 v64, 16, v62
	global_store_dwordx2 v[70:71], v[58:59], off offset:32
	v_lshlrev_b32_e32 v58, 16, v60
	v_and_b32_e32 v59, 0xffff0000, v60
	v_lshlrev_b32_e32 v60, 16, v61
	v_and_b32_e32 v61, 0xffff0000, v61
	v_and_b32_e32 v65, 0xffff0000, v62
	v_lshlrev_b32_e32 v62, 16, v63
	v_and_b32_e32 v63, 0xffff0000, v63
	v_pk_fma_f32 v[56:57], v[56:57], v[60:61], v[62:63]
	v_pk_fma_f32 v[54:55], v[54:55], v[58:59], v[64:65]
	v_add_u32_e32 v60, 0x90, v144
	v_cvt_pk_bf16_f32 v54, v54, v55
	v_cvt_pk_bf16_f32 v55, v56, v57
	v_mov_b32_e32 v56, v200
	v_mov_b32_e32 v57, v201
	v_mov_b32_e32 v58, v202
	v_mov_b32_e32 v59, v203
	v_ashrrev_i32_e32 v61, 31, v60
	v_mad_i64_i32 v[62:63], s[22:23], v60, s48, v[146:147]
	global_store_dwordx2 v[70:71], v[54:55], off offset:256
	v_lshl_add_u64 v[62:63], v[62:63], 0, v[142:143]
	v_add_co_u32_e32 v64, vcc, s49, v62
	s_nop 0
	v_lshlrev_b32_e32 v54, 16, v56
	v_and_b32_e32 v55, 0xffff0000, v56
	v_lshlrev_b32_e32 v66, 16, v58
	v_and_b32_e32 v67, 0xffff0000, v58
	v_pk_fma_f32 v[50:51], v[50:51], v[54:55], v[66:67]
	v_lshlrev_b64 v[54:55], 12, v[60:61]
	v_lshlrev_b32_e32 v56, 16, v57
	v_and_b32_e32 v57, 0xffff0000, v57
	v_lshlrev_b32_e32 v58, 16, v59
	v_and_b32_e32 v59, 0xffff0000, v59
	v_lshl_add_u64 v[54:55], s[8:9], 0, v[54:55]
	v_addc_co_u32_e32 v65, vcc, 0, v63, vcc
	v_pk_fma_f32 v[52:53], v[52:53], v[56:57], v[58:59]
	v_lshl_add_u64 v[54:55], v[54:55], 0, v[142:143]
	v_cvt_pk_bf16_f32 v50, v50, v51
	v_cvt_pk_bf16_f32 v51, v52, v53
	v_mov_b32_e32 v52, v204
	v_mov_b32_e32 v53, v205
	v_mov_b32_e32 v56, v206
	v_mov_b32_e32 v57, v207
	v_lshl_add_u64 v[58:59], v[62:63], 0, s[10:11]
	global_store_dwordx2 v[70:71], v[50:51], off offset:288
	s_nop 0
	v_lshlrev_b32_e32 v50, 16, v52
	v_and_b32_e32 v51, 0xffff0000, v52
	v_lshlrev_b32_e32 v52, 16, v53
	v_and_b32_e32 v53, 0xffff0000, v53
	v_lshlrev_b32_e32 v60, 16, v56
	v_and_b32_e32 v61, 0xffff0000, v56
	v_lshlrev_b32_e32 v56, 16, v57
	v_and_b32_e32 v57, 0xffff0000, v57
	v_pk_fma_f32 v[48:49], v[48:49], v[52:53], v[56:57]
	v_pk_fma_f32 v[46:47], v[46:47], v[50:51], v[60:61]
	s_nop 0
	v_cvt_pk_bf16_f32 v46, v46, v47
	v_cvt_pk_bf16_f32 v47, v48, v49
	v_mov_b32_e32 v48, v208
	v_mov_b32_e32 v49, v209
	v_mov_b32_e32 v50, v210
	v_mov_b32_e32 v51, v211
	s_nop 0
	v_lshlrev_b32_e32 v52, 16, v50
	global_store_dwordx2 v[54:55], v[46:47], off
	v_lshlrev_b32_e32 v46, 16, v48
	v_and_b32_e32 v47, 0xffff0000, v48
	v_lshlrev_b32_e32 v48, 16, v49
	v_and_b32_e32 v49, 0xffff0000, v49
	v_and_b32_e32 v53, 0xffff0000, v50
	v_lshlrev_b32_e32 v50, 16, v51
	v_and_b32_e32 v51, 0xffff0000, v51
	v_pk_fma_f32 v[44:45], v[44:45], v[48:49], v[50:51]
	v_pk_fma_f32 v[42:43], v[42:43], v[46:47], v[52:53]
	s_nop 0
	v_cvt_pk_bf16_f32 v42, v42, v43
	v_cvt_pk_bf16_f32 v43, v44, v45
	v_mov_b32_e32 v44, v212
	v_mov_b32_e32 v45, v213
	v_mov_b32_e32 v46, v214
	v_mov_b32_e32 v47, v215
	s_nop 0
	v_lshlrev_b32_e32 v48, 16, v46
	global_store_dwordx2 v[54:55], v[42:43], off offset:32
	v_lshlrev_b32_e32 v42, 16, v44
	v_and_b32_e32 v43, 0xffff0000, v44
	v_lshlrev_b32_e32 v44, 16, v45
	v_and_b32_e32 v45, 0xffff0000, v45
	v_and_b32_e32 v49, 0xffff0000, v46
	v_lshlrev_b32_e32 v46, 16, v47
	v_and_b32_e32 v47, 0xffff0000, v47
	v_pk_fma_f32 v[40:41], v[40:41], v[44:45], v[46:47]
	v_pk_fma_f32 v[38:39], v[38:39], v[42:43], v[48:49]
	v_add_u32_e32 v44, 0xa0, v144
	v_cvt_pk_bf16_f32 v38, v38, v39
	v_cvt_pk_bf16_f32 v39, v40, v41
	v_mov_b32_e32 v40, v216
	v_mov_b32_e32 v41, v217
	v_mov_b32_e32 v42, v218
	v_mov_b32_e32 v43, v219
	v_ashrrev_i32_e32 v45, 31, v44
	v_mad_i64_i32 v[46:47], s[22:23], v44, s48, v[146:147]
	global_store_dwordx2 v[54:55], v[38:39], off offset:256
	v_lshl_add_u64 v[46:47], v[46:47], 0, v[142:143]
	v_add_co_u32_e32 v48, vcc, s49, v46
	s_nop 0
	v_lshlrev_b32_e32 v38, 16, v40
	v_and_b32_e32 v39, 0xffff0000, v40
	v_lshlrev_b32_e32 v50, 16, v42
	v_and_b32_e32 v51, 0xffff0000, v42
	v_pk_fma_f32 v[34:35], v[34:35], v[38:39], v[50:51]
	v_lshlrev_b64 v[38:39], 12, v[44:45]
	v_lshlrev_b32_e32 v40, 16, v41
	v_and_b32_e32 v41, 0xffff0000, v41
	v_lshlrev_b32_e32 v42, 16, v43
	v_and_b32_e32 v43, 0xffff0000, v43
	v_lshl_add_u64 v[38:39], s[8:9], 0, v[38:39]
	v_addc_co_u32_e32 v49, vcc, 0, v47, vcc
	v_pk_fma_f32 v[36:37], v[36:37], v[40:41], v[42:43]
	v_lshl_add_u64 v[38:39], v[38:39], 0, v[142:143]
	v_cvt_pk_bf16_f32 v34, v34, v35
	v_cvt_pk_bf16_f32 v35, v36, v37
	v_mov_b32_e32 v237, 0x1000
	v_mov_b32_e32 v236, 160
	v_mad_i64_i32 v[230:231], s[22:23], v236, s48, v[228:229]
	v_mad_i64_i32 v[234:235], s[22:23], v236, v237, v[232:233]
	global_load_dwordx2 v[168:169], v[230:231], off
	global_load_dwordx2 v[170:171], v[234:235], off
	global_load_dwordx2 v[172:173], v[230:231], off offset:32
	global_load_dwordx2 v[174:175], v[234:235], off offset:32
	global_load_dwordx2 v[176:177], v[230:231], off offset:256
	global_load_dwordx2 v[178:179], v[234:235], off offset:256
	global_load_dwordx2 v[180:181], v[230:231], off offset:288
	global_load_dwordx2 v[182:183], v[234:235], off offset:288
	v_mov_b32_e32 v236, 176
	v_mad_i64_i32 v[230:231], s[22:23], v236, s48, v[228:229]
	v_mad_i64_i32 v[234:235], s[22:23], v236, v237, v[232:233]
	global_load_dwordx2 v[184:185], v[230:231], off
	global_load_dwordx2 v[186:187], v[234:235], off
	global_load_dwordx2 v[192:193], v[230:231], off offset:32
	global_load_dwordx2 v[194:195], v[234:235], off offset:32
	global_load_dwordx2 v[196:197], v[230:231], off offset:256
	global_load_dwordx2 v[198:199], v[234:235], off offset:256
	global_load_dwordx2 v[200:201], v[230:231], off offset:288
	global_load_dwordx2 v[202:203], v[234:235], off offset:288
	s_waitcnt vmcnt(0)
	v_mov_b32_e32 v36, v168
	v_mov_b32_e32 v37, v169
	v_mov_b32_e32 v40, v170
	v_mov_b32_e32 v41, v171
	v_lshl_add_u64 v[42:43], v[46:47], 0, s[10:11]
	global_store_dwordx2 v[54:55], v[34:35], off offset:288
	s_nop 0
	v_lshlrev_b32_e32 v34, 16, v36
	v_and_b32_e32 v35, 0xffff0000, v36
	v_lshlrev_b32_e32 v36, 16, v37
	v_and_b32_e32 v37, 0xffff0000, v37
	v_lshlrev_b32_e32 v44, 16, v40
	v_and_b32_e32 v45, 0xffff0000, v40
	v_lshlrev_b32_e32 v40, 16, v41
	v_and_b32_e32 v41, 0xffff0000, v41
	v_pk_fma_f32 v[32:33], v[32:33], v[36:37], v[40:41]
	v_pk_fma_f32 v[30:31], v[30:31], v[34:35], v[44:45]
	s_nop 0
	v_cvt_pk_bf16_f32 v30, v30, v31
	v_cvt_pk_bf16_f32 v31, v32, v33
	v_mov_b32_e32 v32, v172
	v_mov_b32_e32 v33, v173
	v_mov_b32_e32 v34, v174
	v_mov_b32_e32 v35, v175
	s_nop 0
	v_lshlrev_b32_e32 v36, 16, v34
	global_store_dwordx2 v[38:39], v[30:31], off
	v_lshlrev_b32_e32 v30, 16, v32
	v_and_b32_e32 v31, 0xffff0000, v32
	v_lshlrev_b32_e32 v32, 16, v33
	v_and_b32_e32 v33, 0xffff0000, v33
	v_and_b32_e32 v37, 0xffff0000, v34
	v_lshlrev_b32_e32 v34, 16, v35
	v_and_b32_e32 v35, 0xffff0000, v35
	v_pk_fma_f32 v[28:29], v[28:29], v[32:33], v[34:35]
	v_pk_fma_f32 v[26:27], v[26:27], v[30:31], v[36:37]
	s_nop 0
	v_cvt_pk_bf16_f32 v26, v26, v27
	v_cvt_pk_bf16_f32 v27, v28, v29
	v_mov_b32_e32 v28, v176
	v_mov_b32_e32 v29, v177
	v_mov_b32_e32 v30, v178
	v_mov_b32_e32 v31, v179
	s_nop 0
	v_lshlrev_b32_e32 v32, 16, v30
	global_store_dwordx2 v[38:39], v[26:27], off offset:32
	v_lshlrev_b32_e32 v26, 16, v28
	v_and_b32_e32 v27, 0xffff0000, v28
	v_lshlrev_b32_e32 v28, 16, v29
	v_and_b32_e32 v29, 0xffff0000, v29
	v_and_b32_e32 v33, 0xffff0000, v30
	v_lshlrev_b32_e32 v30, 16, v31
	v_and_b32_e32 v31, 0xffff0000, v31
	v_pk_fma_f32 v[24:25], v[24:25], v[28:29], v[30:31]
	v_pk_fma_f32 v[22:23], v[22:23], v[26:27], v[32:33]
	v_add_u32_e32 v28, 0xb0, v144
	v_cvt_pk_bf16_f32 v22, v22, v23
	v_cvt_pk_bf16_f32 v23, v24, v25
	v_mov_b32_e32 v24, v180
	v_mov_b32_e32 v25, v181
	v_mov_b32_e32 v26, v182
	v_mov_b32_e32 v27, v183
	v_ashrrev_i32_e32 v29, 31, v28
	v_mad_i64_i32 v[30:31], s[22:23], v28, s48, v[146:147]
	global_store_dwordx2 v[38:39], v[22:23], off offset:256
	v_lshl_add_u64 v[30:31], v[30:31], 0, v[142:143]
	v_add_co_u32_e32 v32, vcc, s49, v30
	s_mov_b64 s[22:23], s[16:17]
	s_nop 0
	v_addc_co_u32_e32 v33, vcc, 0, v31, vcc
	s_and_b64 vcc, exec, s[0:1]
	s_nop 0
	v_lshlrev_b32_e32 v22, 16, v24
	v_and_b32_e32 v23, 0xffff0000, v24
	v_lshlrev_b32_e32 v34, 16, v26
	v_and_b32_e32 v35, 0xffff0000, v26
	v_pk_fma_f32 v[18:19], v[18:19], v[22:23], v[34:35]
	v_lshlrev_b64 v[22:23], 12, v[28:29]
	v_lshlrev_b32_e32 v24, 16, v25
	v_and_b32_e32 v25, 0xffff0000, v25
	v_lshlrev_b32_e32 v26, 16, v27
	v_and_b32_e32 v27, 0xffff0000, v27
	v_lshl_add_u64 v[22:23], s[8:9], 0, v[22:23]
	v_pk_fma_f32 v[20:21], v[20:21], v[24:25], v[26:27]
	v_lshl_add_u64 v[22:23], v[22:23], 0, v[142:143]
	v_cvt_pk_bf16_f32 v18, v18, v19
	v_cvt_pk_bf16_f32 v19, v20, v21
	v_mov_b32_e32 v20, v184
	v_mov_b32_e32 v21, v185
	v_mov_b32_e32 v24, v186
	v_mov_b32_e32 v25, v187
	v_lshl_add_u64 v[26:27], v[30:31], 0, s[10:11]
	global_store_dwordx2 v[38:39], v[18:19], off offset:288
	s_nop 0
	v_lshlrev_b32_e32 v18, 16, v20
	v_and_b32_e32 v19, 0xffff0000, v20
	v_lshlrev_b32_e32 v20, 16, v21
	v_and_b32_e32 v21, 0xffff0000, v21
	v_lshlrev_b32_e32 v28, 16, v24
	v_and_b32_e32 v29, 0xffff0000, v24
	v_lshlrev_b32_e32 v24, 16, v25
	v_and_b32_e32 v25, 0xffff0000, v25
	v_pk_fma_f32 v[16:17], v[16:17], v[20:21], v[24:25]
	v_pk_fma_f32 v[14:15], v[14:15], v[18:19], v[28:29]
	s_nop 0
	v_cvt_pk_bf16_f32 v14, v14, v15
	v_cvt_pk_bf16_f32 v15, v16, v17
	v_mov_b32_e32 v16, v192
	v_mov_b32_e32 v17, v193
	v_mov_b32_e32 v18, v194
	v_mov_b32_e32 v19, v195
	s_nop 0
	v_lshlrev_b32_e32 v20, 16, v18
	global_store_dwordx2 v[22:23], v[14:15], off
	v_lshlrev_b32_e32 v14, 16, v16
	v_and_b32_e32 v15, 0xffff0000, v16
	v_lshlrev_b32_e32 v16, 16, v17
	v_and_b32_e32 v17, 0xffff0000, v17
	v_and_b32_e32 v21, 0xffff0000, v18
	v_lshlrev_b32_e32 v18, 16, v19
	v_and_b32_e32 v19, 0xffff0000, v19
	v_pk_fma_f32 v[12:13], v[12:13], v[16:17], v[18:19]
	v_pk_fma_f32 v[10:11], v[10:11], v[14:15], v[20:21]
	s_nop 0
	v_cvt_pk_bf16_f32 v10, v10, v11
	v_cvt_pk_bf16_f32 v11, v12, v13
	v_mov_b32_e32 v12, v196
	v_mov_b32_e32 v13, v197
	v_mov_b32_e32 v14, v198
	v_mov_b32_e32 v15, v199
	s_nop 0
	v_lshlrev_b32_e32 v16, 16, v14
	global_store_dwordx2 v[22:23], v[10:11], off offset:32
	v_lshlrev_b32_e32 v10, 16, v12
	v_and_b32_e32 v11, 0xffff0000, v12
	v_lshlrev_b32_e32 v12, 16, v13
	v_and_b32_e32 v13, 0xffff0000, v13
	v_and_b32_e32 v17, 0xffff0000, v14
	v_lshlrev_b32_e32 v14, 16, v15
	v_and_b32_e32 v15, 0xffff0000, v15
	v_pk_fma_f32 v[8:9], v[8:9], v[12:13], v[14:15]
	v_pk_fma_f32 v[6:7], v[6:7], v[10:11], v[16:17]
	s_nop 0
	v_cvt_pk_bf16_f32 v6, v6, v7
	v_cvt_pk_bf16_f32 v7, v8, v9
	v_mov_b32_e32 v8, v200
	v_mov_b32_e32 v9, v201
	v_mov_b32_e32 v10, v202
	v_mov_b32_e32 v11, v203
	s_nop 0
	v_lshlrev_b32_e32 v12, 16, v10
	global_store_dwordx2 v[22:23], v[6:7], off offset:256
	v_lshlrev_b32_e32 v6, 16, v8
	v_and_b32_e32 v7, 0xffff0000, v8
	v_and_b32_e32 v13, 0xffff0000, v10
	v_lshlrev_b32_e32 v8, 16, v9
	v_and_b32_e32 v9, 0xffff0000, v9
	v_lshlrev_b32_e32 v10, 16, v11
	v_and_b32_e32 v11, 0xffff0000, v11
	v_pk_fma_f32 v[2:3], v[2:3], v[6:7], v[12:13]
	v_pk_fma_f32 v[4:5], v[4:5], v[8:9], v[10:11]
	v_cvt_pk_bf16_f32 v2, v2, v3
	s_nop 0
	v_cvt_pk_bf16_f32 v3, v4, v5
	global_store_dwordx2 v[22:23], v[2:3], off offset:288
	s_cbranch_vccz .LBB0_1220
	s_waitcnt vmcnt(0)
	s_cmpk_gt_u32 s28, 0xff
	s_cbranch_scc1 .LBB0_1227
	s_barrier
